# speedup vs baseline: 1.0350x; 1.0350x over previous
.LBB0_52:
	s_or_b64 exec, exec, s[6:7]
	v_lshlrev_b32_e32 v2, 3, v0
	s_waitcnt lgkmcnt(0)
	s_barrier
	ds_read2st64_b64 v[8:11], v2 offset1:8
	s_lshl_b64 s[6:7], s[26:27], 3
	s_add_u32 s6, s30, s6
	s_addc_u32 s7, s31, s7
	v_mov_b32_e32 v3, 0
	v_lshl_add_u64 v[4:5], s[6:7], 0, v[2:3]
	s_movk_i32 s3, 0x1000
	s_waitcnt lgkmcnt(0)
	global_store_dwordx2 v2, v[8:9], s[6:7] sc1
	v_add_co_u32_e32 v8, vcc, s3, v4
	v_lshlrev_b32_e32 v3, 3, v7
	s_nop 0
	v_addc_co_u32_e32 v9, vcc, 0, v5, vcc
	global_store_dwordx2 v[8:9], v[10:11], off sc1
	ds_read2st64_b64 v[6:9], v2 offset0:32 offset1:40
	ds_read2st64_b64 v[12:15], v2 offset0:16 offset1:24
	s_movk_i32 s3, 0x3000
	v_add_co_u32_e32 v10, vcc, s3, v4
	v_lshlrev_b32_e32 v1, 3, v1
	s_nop 0
	v_addc_co_u32_e32 v11, vcc, 0, v5, vcc
	s_waitcnt lgkmcnt(1)
	global_store_dwordx2 v1, v[6:7], s[6:7] sc1
	v_add_co_u32_e32 v6, vcc, 0x5000, v4
	s_waitcnt lgkmcnt(0)
	global_store_dwordx2 v3, v[12:13], s[6:7] sc1
	v_addc_co_u32_e32 v7, vcc, 0, v5, vcc
	global_store_dwordx2 v[10:11], v[14:15], off sc1
	global_store_dwordx2 v[6:7], v[8:9], off sc1
	s_and_saveexec_b64 s[8:9], s[22:23]
	s_cbranch_execz .LBB0_54
	ds_read_b64 v[6:7], v2 offset:24576
	v_lshlrev_b32_e32 v1, 3, v20
	s_waitcnt lgkmcnt(0)
	global_store_dwordx2 v1, v[6:7], s[6:7] sc1
.LBB0_54:
	s_or_b64 exec, exec, s[8:9]
	s_and_saveexec_b64 s[6:7], s[4:5]
	s_cbranch_execz .LBB0_56
	ds_read_b64 v[2:3], v2 offset:28672
	v_add_co_u32_e32 v4, vcc, 0x7000, v4
	s_nop 1
	v_addc_co_u32_e32 v5, vcc, 0, v5, vcc
	s_waitcnt lgkmcnt(0)
	global_store_dwordx2 v[4:5], v[2:3], off sc1

_Z11k_csr_gemm1PKjPK15HIP_vector_typeIiLj2EEPS2_PiS6_PfS6_PKfPKDv8_DF16_PDF16_:
	s_mov_b64 s[4:5], -1
	s_cmpk_gt_u32 s2, 0x186
	v_lshrrev_b32_e32 v1, 6, v0
	v_and_b32_e32 v88, 63, v0
	s_cbranch_scc0 .LBB1_42
	s_load_dwordx4 s[4:7], s[0:1], 0x38
	v_lshlrev_b32_e32 v82, 4, v0
	v_mov_b32_e32 v83, 0
	s_lshl_b32 s3, s2, 6
	v_lshrrev_b32_e32 v89, 6, v0
	s_waitcnt lgkmcnt(0)
	v_lshl_add_u64 v[6:7], s[6:7], 0, v[82:83]
	v_add_co_u32_e32 v2, vcc, 0x1000, v6
	s_addk_i32 s3, 0x9e40
	s_nop 0
	v_addc_co_u32_e32 v3, vcc, 0, v7, vcc
	v_add_co_u32_e32 v4, vcc, 0x2000, v6
	v_or_b32_e32 v86, s3, v89
	s_nop 0
	v_addc_co_u32_e32 v5, vcc, 0, v7, vcc
	global_load_dwordx4 v[58:61], v[2:3], off
	global_load_dwordx4 v[34:37], v[4:5], off
	v_add_co_u32_e32 v2, vcc, 0x3000, v6
	v_ashrrev_i32_e32 v87, 31, v86
	s_nop 0
	v_addc_co_u32_e32 v3, vcc, 0, v7, vcc
	v_add_co_u32_e32 v4, vcc, 0x4000, v6
	v_mov_b32_e32 v68, 0
	s_nop 0
	v_addc_co_u32_e32 v5, vcc, 0, v7, vcc
	global_load_dwordx4 v[54:57], v[2:3], off
	global_load_dwordx4 v[30:33], v[4:5], off
	v_add_co_u32_e32 v2, vcc, 0x5000, v6
	v_mov_b32_e32 v69, 0
	s_nop 0
	v_addc_co_u32_e32 v3, vcc, 0, v7, vcc
	v_add_co_u32_e32 v4, vcc, 0x6000, v6
	s_nop 1
	v_addc_co_u32_e32 v5, vcc, 0, v7, vcc
	global_load_dwordx4 v[50:53], v[2:3], off
	global_load_dwordx4 v[26:29], v[4:5], off
	v_add_co_u32_e32 v2, vcc, 0x7000, v6
	s_nop 1
	v_addc_co_u32_e32 v3, vcc, 0, v7, vcc
	v_add_co_u32_e32 v4, vcc, 0x8000, v6
	s_nop 1
	v_addc_co_u32_e32 v5, vcc, 0, v7, vcc
	global_load_dwordx4 v[46:49], v[2:3], off
	global_load_dwordx4 v[22:25], v[4:5], off
	v_add_co_u32_e32 v2, vcc, 0x9000, v6
	s_nop 1
	v_addc_co_u32_e32 v3, vcc, 0, v7, vcc
	v_add_co_u32_e32 v4, vcc, 0xa000, v6
	s_nop 1
	v_addc_co_u32_e32 v5, vcc, 0, v7, vcc
	global_load_dwordx4 v[42:45], v[2:3], off
	global_load_dwordx4 v[18:21], v[4:5], off
	v_add_co_u32_e32 v2, vcc, 0xb000, v6
	s_nop 1
	v_addc_co_u32_e32 v3, vcc, 0, v7, vcc
	v_add_co_u32_e32 v4, vcc, 0xc000, v6
	s_nop 1
	v_addc_co_u32_e32 v5, vcc, 0, v7, vcc
	v_add_co_u32_e32 v8, vcc, 0xd000, v6
	global_load_dwordx4 v[38:41], v[2:3], off
	global_load_dwordx4 v[14:17], v[4:5], off
	v_addc_co_u32_e32 v9, vcc, 0, v7, vcc
	v_add_co_u32_e32 v62, vcc, 0xe000, v6
	s_nop 1
	v_addc_co_u32_e32 v63, vcc, 0, v7, vcc
	v_add_co_u32_e32 v66, vcc, 0xf000, v6
	global_load_dwordx4 v[10:13], v[8:9], off
	global_load_dwordx4 v[2:5], v[62:63], off
	v_addc_co_u32_e32 v67, vcc, 0, v7, vcc
	global_load_dwordx4 v[62:65], v82, s[6:7]
	global_load_dwordx4 v[6:9], v[66:67], off
	v_lshlrev_b32_e32 v66, 4, v88
	v_mov_b32_e32 v67, 0
	v_lshl_add_u64 v[84:85], s[4:5], 0, v[66:67]
	s_load_dwordx2 s[4:5], s[0:1], 0x48
	s_movk_i32 s8, 0x400
	s_mov_b32 s9, 0xc34f
	s_movk_i32 s10, 0x210
	v_lshlrev_b32_e32 v90, 3, v88
	v_mad_u32_u24 v83, v89, s10, v90
	v_min_u32_e32 v92, s9, v86
	v_mad_u64_u32 v[92:93], s[12:13], v92, s8, v[84:85]
	global_load_dwordx4 v[66:69], v[92:93], off nt
	v_add_u32_e32 v94, 4, v86
	v_min_u32_e32 v94, s9, v94
	v_mad_u64_u32 v[94:95], s[12:13], v94, s8, v[84:85]
	global_load_dwordx4 v[70:73], v[94:95], off nt
	v_add_u32_e32 v92, 8, v86
	v_min_u32_e32 v92, s9, v92
	v_mad_u64_u32 v[92:93], s[12:13], v92, s8, v[84:85]
	global_load_dwordx4 v[74:77], v[92:93], off nt
	v_add_u32_e32 v94, 12, v86
	v_min_u32_e32 v94, s9, v94
	v_mad_u64_u32 v[94:95], s[12:13], v94, s8, v[84:85]
	global_load_dwordx4 v[78:81], v[94:95], off nt
	v_add_u32_e32 v92, 16, v86
	v_min_u32_e32 v92, s9, v92
	v_mad_u64_u32 v[92:93], s[12:13], v92, s8, v[84:85]
	global_load_dwordx4 a[0:3], v[92:93], off nt
	v_add_u32_e32 v94, 20, v86
	v_min_u32_e32 v94, s9, v94
	v_mad_u64_u32 v[94:95], s[12:13], v94, s8, v[84:85]
	global_load_dwordx4 a[4:7], v[94:95], off nt
	v_add_u32_e32 v92, 24, v86
	v_min_u32_e32 v92, s9, v92
	v_mad_u64_u32 v[92:93], s[12:13], v92, s8, v[84:85]
	global_load_dwordx4 a[8:11], v[92:93], off nt
	v_add_u32_e32 v94, 28, v86
	v_min_u32_e32 v94, s9, v94
	v_mad_u64_u32 v[94:95], s[12:13], v94, s8, v[84:85]
	global_load_dwordx4 a[12:15], v[94:95], off nt
	v_add_u32_e32 v92, 32, v86
	v_min_u32_e32 v92, s9, v92
	v_mad_u64_u32 v[92:93], s[12:13], v92, s8, v[84:85]
	global_load_dwordx4 a[16:19], v[92:93], off nt
	v_add_u32_e32 v94, 36, v86
	v_min_u32_e32 v94, s9, v94
	v_mad_u64_u32 v[94:95], s[12:13], v94, s8, v[84:85]
	global_load_dwordx4 a[20:23], v[94:95], off nt
	v_add_u32_e32 v92, 40, v86
	v_min_u32_e32 v92, s9, v92
	v_mad_u64_u32 v[92:93], s[12:13], v92, s8, v[84:85]
	global_load_dwordx4 a[24:27], v[92:93], off nt
	v_add_u32_e32 v94, 44, v86
	v_min_u32_e32 v94, s9, v94
	v_mad_u64_u32 v[94:95], s[12:13], v94, s8, v[84:85]
	global_load_dwordx4 a[28:31], v[94:95], off nt
	s_waitcnt vmcnt(11)
	v_cvt_pk_f16_f32 v66, v66, v67
	v_cvt_pk_f16_f32 v67, v68, v69
	ds_write_b64 v83, v[66:67]
	s_waitcnt vmcnt(10)
	v_cvt_pk_f16_f32 v70, v70, v71
	v_cvt_pk_f16_f32 v71, v72, v73
	ds_write_b64 v83, v[70:71] offset:2112
	s_waitcnt vmcnt(9)
	v_cvt_pk_f16_f32 v74, v74, v75
	v_cvt_pk_f16_f32 v75, v76, v77
	ds_write_b64 v83, v[74:75] offset:4224
	s_waitcnt vmcnt(8)
	v_cvt_pk_f16_f32 v78, v78, v79
	v_cvt_pk_f16_f32 v79, v80, v81
	ds_write_b64 v83, v[78:79] offset:6336
	v_add_u32_e32 v92, 48, v86
	v_min_u32_e32 v92, s9, v92
	v_mad_u64_u32 v[92:93], s[12:13], v92, s8, v[84:85]
	global_load_dwordx4 v[66:69], v[92:93], off nt
	v_add_u32_e32 v94, 52, v86
	v_min_u32_e32 v94, s9, v94
	v_mad_u64_u32 v[94:95], s[12:13], v94, s8, v[84:85]
	global_load_dwordx4 v[70:73], v[94:95], off nt
	v_add_u32_e32 v92, 56, v86
	v_min_u32_e32 v92, s9, v92
	v_mad_u64_u32 v[92:93], s[12:13], v92, s8, v[84:85]
	global_load_dwordx4 v[74:77], v[92:93], off nt
	v_add_u32_e32 v94, 60, v86
	v_min_u32_e32 v94, s9, v94
	v_mad_u64_u32 v[94:95], s[12:13], v94, s8, v[84:85]
	global_load_dwordx4 v[78:81], v[94:95], off nt
	s_waitcnt vmcnt(11)
	v_accvgpr_read_b32 v92, a0
	v_accvgpr_read_b32 v93, a1
	v_accvgpr_read_b32 v94, a2
	v_accvgpr_read_b32 v95, a3
	v_cvt_pk_f16_f32 v92, v92, v93
	v_cvt_pk_f16_f32 v93, v94, v95
	ds_write_b64 v83, v[92:93] offset:8448
	s_waitcnt vmcnt(10)
	v_accvgpr_read_b32 v92, a4
	v_accvgpr_read_b32 v93, a5
	v_accvgpr_read_b32 v94, a6
	v_accvgpr_read_b32 v95, a7
	v_cvt_pk_f16_f32 v92, v92, v93
	v_cvt_pk_f16_f32 v93, v94, v95
	ds_write_b64 v83, v[92:93] offset:10560
	s_waitcnt vmcnt(9)
	v_accvgpr_read_b32 v92, a8
	v_accvgpr_read_b32 v93, a9
	v_accvgpr_read_b32 v94, a10
	v_accvgpr_read_b32 v95, a11
	v_cvt_pk_f16_f32 v92, v92, v93
	v_cvt_pk_f16_f32 v93, v94, v95
	ds_write_b64 v83, v[92:93] offset:12672
	s_waitcnt vmcnt(8)
	v_accvgpr_read_b32 v92, a12
	v_accvgpr_read_b32 v93, a13
	v_accvgpr_read_b32 v94, a14
	v_accvgpr_read_b32 v95, a15
	v_cvt_pk_f16_f32 v92, v92, v93
	v_cvt_pk_f16_f32 v93, v94, v95
	ds_write_b64 v83, v[92:93] offset:14784
	s_waitcnt vmcnt(7)
	v_accvgpr_read_b32 v92, a16
	v_accvgpr_read_b32 v93, a17
	v_accvgpr_read_b32 v94, a18
	v_accvgpr_read_b32 v95, a19
	v_cvt_pk_f16_f32 v92, v92, v93
	v_cvt_pk_f16_f32 v93, v94, v95
	ds_write_b64 v83, v[92:93] offset:16896
	s_waitcnt vmcnt(6)
	v_accvgpr_read_b32 v92, a20
	v_accvgpr_read_b32 v93, a21
	v_accvgpr_read_b32 v94, a22
	v_accvgpr_read_b32 v95, a23
	v_cvt_pk_f16_f32 v92, v92, v93
	v_cvt_pk_f16_f32 v93, v94, v95
	ds_write_b64 v83, v[92:93] offset:19008
	s_waitcnt vmcnt(5)
	v_accvgpr_read_b32 v92, a24
	v_accvgpr_read_b32 v93, a25
	v_accvgpr_read_b32 v94, a26
	v_accvgpr_read_b32 v95, a27
	v_cvt_pk_f16_f32 v92, v92, v93
	v_cvt_pk_f16_f32 v93, v94, v95
	ds_write_b64 v83, v[92:93] offset:21120
	s_waitcnt vmcnt(4)
	v_accvgpr_read_b32 v92, a28
	v_accvgpr_read_b32 v93, a29
	v_accvgpr_read_b32 v94, a30
	v_accvgpr_read_b32 v95, a31
	v_cvt_pk_f16_f32 v92, v92, v93
	v_cvt_pk_f16_f32 v93, v94, v95
	ds_write_b64 v83, v[92:93] offset:23232
	s_waitcnt vmcnt(3)
	v_cvt_pk_f16_f32 v66, v66, v67
	v_cvt_pk_f16_f32 v67, v68, v69
	ds_write_b64 v83, v[66:67] offset:25344
	s_waitcnt vmcnt(2)
	v_cvt_pk_f16_f32 v70, v70, v71
	v_cvt_pk_f16_f32 v71, v72, v73
	ds_write_b64 v83, v[70:71] offset:27456
	s_waitcnt vmcnt(1)
	v_cvt_pk_f16_f32 v74, v74, v75
	v_cvt_pk_f16_f32 v75, v76, v77
	ds_write_b64 v83, v[74:75] offset:29568
	s_waitcnt vmcnt(0)
	v_cvt_pk_f16_f32 v78, v78, v79
	v_cvt_pk_f16_f32 v79, v80, v81
	ds_write_b64 v83, v[78:79] offset:31680
	v_and_b32_e32 v78, 31, v0
	v_lshrrev_b32_e32 v66, 2, v0
	v_and_b32_e32 v79, 8, v66
	v_mul_u32_u24_e32 v66, 0x210, v78
	v_lshl_add_u32 v80, v79, 1, v66
	s_waitcnt lgkmcnt(0)
	s_barrier
	ds_read_b128 v[66:69], v80
	ds_read_b128 v[70:73], v80 offset:32
	s_waitcnt lgkmcnt(1)
	v_mfma_f32_32x32x16_f16 a[16:31], v[62:65], v[66:69], 0
	ds_read_b128 v[66:69], v80 offset:16896
	ds_read_b128 v[74:77], v80 offset:16928
	s_movk_i32 s6, 0xc0
	s_mov_b32 s7, 0xc350
	s_waitcnt lgkmcnt(1)
	v_mfma_f32_32x32x16_f16 a[0:15], v[62:65], v[66:69], 0
	v_mfma_f32_32x32x16_f16 a[16:31], v[58:61], v[70:73], a[16:31]
	s_waitcnt lgkmcnt(0)
	v_mfma_f32_32x32x16_f16 a[0:15], v[58:61], v[74:77], a[0:15]
	ds_read_b128 v[58:61], v80 offset:64
	ds_read_b128 v[62:65], v80 offset:96
	s_waitcnt lgkmcnt(1)
	v_mfma_f32_32x32x16_f16 a[16:31], v[34:37], v[58:61], a[16:31]
	ds_read_b128 v[58:61], v80 offset:16960
	ds_read_b128 v[66:69], v80 offset:16992
	s_waitcnt lgkmcnt(1)
	v_mfma_f32_32x32x16_f16 a[0:15], v[34:37], v[58:61], a[0:15]
	v_mfma_f32_32x32x16_f16 a[16:31], v[54:57], v[62:65], a[16:31]
	s_waitcnt lgkmcnt(0)
	v_mfma_f32_32x32x16_f16 a[0:15], v[54:57], v[66:69], a[0:15]
	ds_read_b128 v[34:37], v80 offset:128
	ds_read_b128 v[54:57], v80 offset:160
	s_waitcnt lgkmcnt(1)
	v_mfma_f32_32x32x16_f16 a[16:31], v[30:33], v[34:37], a[16:31]
	ds_read_b128 v[34:37], v80 offset:17024
	ds_read_b128 v[58:61], v80 offset:17056
	s_waitcnt lgkmcnt(1)
	v_mfma_f32_32x32x16_f16 a[0:15], v[30:33], v[34:37], a[0:15]
	ds_read_b128 v[30:33], v80 offset:192
	ds_read_b128 v[34:37], v80 offset:224
	v_mfma_f32_32x32x16_f16 a[16:31], v[50:53], v[54:57], a[16:31]
	s_waitcnt lgkmcnt(2)
	v_mfma_f32_32x32x16_f16 a[0:15], v[50:53], v[58:61], a[0:15]
	s_waitcnt lgkmcnt(1)
	v_mfma_f32_32x32x16_f16 a[16:31], v[26:29], v[30:33], a[16:31]
	ds_read_b128 v[30:33], v80 offset:17088
	ds_read_b128 v[50:53], v80 offset:17120
	s_waitcnt lgkmcnt(1)
	v_mfma_f32_32x32x16_f16 a[0:15], v[26:29], v[30:33], a[0:15]
	ds_read_b128 v[26:29], v80 offset:256
	ds_read_b128 v[30:33], v80 offset:288
	v_mfma_f32_32x32x16_f16 a[16:31], v[46:49], v[34:37], a[16:31]
	s_waitcnt lgkmcnt(2)
	v_mfma_f32_32x32x16_f16 a[0:15], v[46:49], v[50:53], a[0:15]
	s_waitcnt lgkmcnt(1)
	v_mfma_f32_32x32x16_f16 a[16:31], v[22:25], v[26:29], a[16:31]
	ds_read_b128 v[26:29], v80 offset:17152
	ds_read_b128 v[34:37], v80 offset:17184
	s_waitcnt lgkmcnt(1)
	v_mfma_f32_32x32x16_f16 a[0:15], v[22:25], v[26:29], a[0:15]
	ds_read_b128 v[22:25], v80 offset:320
	ds_read_b128 v[26:29], v80 offset:352
	v_mfma_f32_32x32x16_f16 a[16:31], v[42:45], v[30:33], a[16:31]
	s_waitcnt lgkmcnt(2)
	v_mfma_f32_32x32x16_f16 a[0:15], v[42:45], v[34:37], a[0:15]
	s_waitcnt lgkmcnt(1)
	v_mfma_f32_32x32x16_f16 a[16:31], v[18:21], v[22:25], a[16:31]
	ds_read_b128 v[22:25], v80 offset:17216
	ds_read_b128 v[30:33], v80 offset:17248
	s_waitcnt lgkmcnt(1)
	v_mfma_f32_32x32x16_f16 a[0:15], v[18:21], v[22:25], a[0:15]
	ds_read_b128 v[18:21], v80 offset:384
	ds_read_b128 v[22:25], v80 offset:416
	v_mfma_f32_32x32x16_f16 a[16:31], v[38:41], v[26:29], a[16:31]
	s_waitcnt lgkmcnt(2)
	v_mfma_f32_32x32x16_f16 a[0:15], v[38:41], v[30:33], a[0:15]
	v_and_or_b32 v38, v0, s6, v79
	s_movk_i32 s6, 0x110
	v_mad_u32_u24 v39, v78, s6, v38
	s_waitcnt lgkmcnt(1)
	v_mfma_f32_32x32x16_f16 a[16:31], v[14:17], v[18:21], a[16:31]
	ds_read_b128 v[18:21], v80 offset:17280
	ds_read_b128 v[26:29], v80 offset:17312
	s_waitcnt lgkmcnt(1)
	v_mfma_f32_32x32x16_f16 a[0:15], v[14:17], v[18:21], a[0:15]
	ds_read_b128 v[14:17], v80 offset:448
	ds_read_b128 v[18:21], v80 offset:480
	v_mfma_f32_32x32x16_f16 a[16:31], v[10:13], v[22:25], a[16:31]
	s_waitcnt lgkmcnt(2)
	v_mfma_f32_32x32x16_f16 a[0:15], v[10:13], v[26:29], a[0:15]
	ds_read_b128 v[10:13], v80 offset:17376
	s_waitcnt lgkmcnt(2)
	v_mfma_f32_32x32x16_f16 a[16:31], v[2:5], v[14:17], a[16:31]
	ds_read_b128 v[14:17], v80 offset:17344
	s_waitcnt lgkmcnt(0)
	s_barrier
	v_mfma_f32_32x32x16_f16 a[0:15], v[2:5], v[14:17], a[0:15]
	v_mfma_f32_32x32x16_f16 a[16:31], v[6:9], v[18:21], a[16:31]
	v_mfma_f32_32x32x16_f16 a[0:15], v[6:9], v[10:13], a[0:15]
	s_nop 10
	v_accvgpr_read_b32 v18, a16
	v_accvgpr_read_b32 v19, a17
	v_accvgpr_read_b32 v20, a18
	v_accvgpr_read_b32 v21, a19
	v_accvgpr_read_b32 v22, a20
	v_accvgpr_read_b32 v23, a21
	v_accvgpr_read_b32 v24, a22
	v_accvgpr_read_b32 v25, a23
	v_accvgpr_read_b32 v26, a24
	v_accvgpr_read_b32 v14, a25
	v_accvgpr_read_b32 v15, a26
	v_accvgpr_read_b32 v16, a27
	v_accvgpr_read_b32 v17, a28
	v_accvgpr_read_b32 v27, a29
	v_accvgpr_read_b32 v28, a30
	v_accvgpr_read_b32 v29, a31
	v_cvt_pk_f16_f32 v3, v20, v21
	v_cvt_pk_f16_f32 v2, v18, v19
	v_cvt_pk_f16_f32 v5, v24, v25
	v_cvt_pk_f16_f32 v4, v22, v23
	ds_write2_b64 v39, v[2:3], v[4:5] offset1:2
	v_cvt_pk_f16_f32 v3, v15, v16
	v_cvt_pk_f16_f32 v2, v26, v14
	v_cvt_pk_f16_f32 v5, v28, v29
	v_cvt_pk_f16_f32 v4, v17, v27
	v_accvgpr_read_b32 v6, a0
	v_accvgpr_read_b32 v7, a1
	v_accvgpr_read_b32 v8, a2
	v_accvgpr_read_b32 v9, a3
	v_accvgpr_read_b32 v10, a4
	v_accvgpr_read_b32 v11, a5
	v_accvgpr_read_b32 v12, a6
	v_accvgpr_read_b32 v13, a7
	ds_write2_b64 v39, v[2:3], v[4:5] offset0:4 offset1:6
	v_or_b32_e32 v2, 32, v88
	v_accvgpr_read_b32 v30, a8
	v_accvgpr_read_b32 v31, a9
	v_accvgpr_read_b32 v32, a10
	v_accvgpr_read_b32 v33, a11
	v_accvgpr_read_b32 v34, a12
	v_accvgpr_read_b32 v35, a13
	v_accvgpr_read_b32 v36, a14
	v_accvgpr_read_b32 v37, a15
	v_mad_u32_u24 v14, v2, s6, v38
	v_cvt_pk_f16_f32 v3, v8, v9
	v_cvt_pk_f16_f32 v2, v6, v7
	v_cvt_pk_f16_f32 v5, v12, v13
	v_cvt_pk_f16_f32 v4, v10, v11
	ds_write2_b64 v14, v[2:3], v[4:5] offset1:2
	v_cvt_pk_f16_f32 v3, v32, v33
	v_cvt_pk_f16_f32 v2, v30, v31
	v_cvt_pk_f16_f32 v5, v36, v37
	v_cvt_pk_f16_f32 v4, v34, v35
	v_lshrrev_b32_e32 v8, 4, v0
	ds_write2_b64 v14, v[2:3], v[4:5] offset0:4 offset1:6
	v_and_b32_e32 v4, 0xf0, v82
	v_mov_b32_e32 v5, 0
	v_or_b32_e32 v6, s3, v8
	v_lshl_add_u64 v[2:3], s[4:5], 0, v[4:5]
	v_cmp_gt_i32_e32 vcc, s7, v6
	s_waitcnt lgkmcnt(0)
	s_barrier
	s_and_saveexec_b64 s[4:5], vcc
	s_cbranch_execz .LBB1_35
	v_ashrrev_i32_e32 v7, 31, v6
	v_mad_u32_u24 v5, v8, s6, v4
	v_lshlrev_b64 v[6:7], 8, v[6:7]
	ds_read_b128 v[10:13], v5
	v_lshl_add_u64 v[6:7], v[2:3], 0, v[6:7]
	s_waitcnt lgkmcnt(0)
	global_store_dwordx4 v[6:7], v[10:13], off sc1
	s_nop 1

.LBB1_67:
	s_or_b64 exec, exec, s[18:19]
	v_mov_b32_e32 v4, 0
	s_waitcnt lgkmcnt(0)
	s_barrier
	ds_read_b32 v2, v4 offset:38720
	s_movk_i32 s3, 0x1001
	v_cmp_gt_i32_e32 vcc, s3, v26
	s_mov_b64 s[18:19], -1
	s_waitcnt lgkmcnt(0)
	s_barrier
	s_cbranch_vccnz .Lcsr_mid
	ds_read_b32 v4, v4 offset:34816
	s_mov_b64 s[18:19], 0
	v_mov_b32_e32 v5, 0x100
	v_mov_b32_e32 v7, 1
	v_mov_b32_e32 v8, 2
	v_mov_b32_e32 v9, v6

.LBB1_80:
	s_waitcnt lgkmcnt(0)
	v_cmp_gt_i32_e32 vcc, v4, v6
	s_nop 1
	v_cndmask_b32_e64 v9, v5, 0, vcc
	v_lshlrev_b32_e32 v11, 2, v9
	ds_read_b32 v11, v11 offset:34304
	v_or_b32_e32 v10, 0x80, v9
	s_waitcnt lgkmcnt(0)
	v_cmp_gt_i32_e32 vcc, v11, v6
	s_nop 1
	v_cndmask_b32_e32 v9, v10, v9, vcc
	v_lshlrev_b32_e32 v11, 2, v9
	ds_read_b32 v11, v11 offset:34048
	v_or_b32_e32 v10, 64, v9
	s_waitcnt lgkmcnt(0)
	v_cmp_gt_i32_e32 vcc, v11, v6
	s_nop 1
	v_cndmask_b32_e32 v9, v10, v9, vcc
	v_lshlrev_b32_e32 v11, 2, v9
	ds_read_b32 v11, v11 offset:33920
	v_or_b32_e32 v10, 32, v9
	s_waitcnt lgkmcnt(0)
	v_cmp_gt_i32_e32 vcc, v11, v6
	s_nop 1
	v_cndmask_b32_e32 v9, v10, v9, vcc
	v_lshlrev_b32_e32 v11, 2, v9
	ds_read_b32 v11, v11 offset:33856
	v_add_u32_e32 v10, 16, v9
	s_waitcnt lgkmcnt(0)
	v_cmp_gt_i32_e32 vcc, v11, v6
	s_nop 1
	v_cndmask_b32_e32 v9, v10, v9, vcc
	v_lshlrev_b32_e32 v11, 2, v9
	ds_read_b32 v11, v11 offset:33824
	v_add_u32_e32 v10, 8, v9
	s_waitcnt lgkmcnt(0)
	v_cmp_gt_i32_e32 vcc, v11, v6
	s_nop 1
	v_cndmask_b32_e32 v9, v10, v9, vcc
	v_lshlrev_b32_e32 v11, 2, v9
	ds_read_b32 v11, v11 offset:33808
	v_add_u32_e32 v10, 4, v9
	s_waitcnt lgkmcnt(0)
	v_cmp_gt_i32_e32 vcc, v11, v6
	s_nop 1
	v_cndmask_b32_e32 v9, v10, v9, vcc
	v_lshlrev_b32_e32 v10, 2, v9
	ds_read_b32 v10, v10 offset:33800
	v_add_u32_e32 v11, 2, v9
	s_waitcnt lgkmcnt(0)
	v_cmp_gt_i32_e32 vcc, v10, v6
	s_nop 1
	v_cndmask_b32_e32 v9, v11, v9, vcc
	v_lshlrev_b32_e32 v10, 2, v9
	ds_read_b32 v10, v10 offset:33796
	v_add_u32_e32 v11, 1, v9
	s_waitcnt lgkmcnt(0)
	v_cmp_gt_i32_e32 vcc, v10, v6
	s_nop 1
	v_cndmask_b32_e32 v9, v11, v9, vcc
	v_lshlrev_b32_e32 v9, 2, v9
	ds_read2st64_b32 v[10:11], v9 offset0:132 offset1:140
	s_waitcnt lgkmcnt(0)
	v_sub_u32_e32 v9, v11, v10
	v_add_u32_e32 v10, v6, v9
	v_ashrrev_i32_e32 v11, 31, v10
	v_lshl_add_u64 v[10:11], v[10:11], 3, s[52:53]
	global_load_dwordx2 v[10:11], v[10:11], off
	v_add_u32_e32 v6, 0x100, v6
	v_cmp_ge_i32_e32 vcc, v6, v26
	s_or_b64 s[18:19], vcc, s[18:19]
	s_waitcnt vmcnt(0)
	v_lshlrev_b32_sdwa v9, v8, sext(v10) dst_sel:DWORD dst_unused:UNUSED_PAD src0_sel:DWORD src1_sel:WORD_1
	ds_read_b32 v12, v9 offset:36640
	ds_add_rtn_u32 v9, v9, v7 offset:37680
	s_waitcnt lgkmcnt(0)
	v_add3_u32 v12, v12, v2, v9
	v_ashrrev_i32_e32 v13, 31, v12
	v_lshl_add_u64 v[12:13], v[12:13], 3, s[54:55]
	global_store_dwordx2 v[12:13], v[10:11], off
	s_andn2_b64 exec, exec, s[18:19]
	s_cbranch_execnz .LBB1_80
	s_or_b64 exec, exec, s[18:19]
	s_endpgm
.Lcsr_mid:
	v_readfirstlane_b32 s33, v26
	v_mov_b32_e32 v27, 0
	v_mov_b32_e32 v28, -1
	v_mov_b32_e32 v30, -1
	v_mov_b32_e32 v32, -1
	v_mov_b32_e32 v34, -1
	v_mov_b32_e32 v36, -1
	v_mov_b32_e32 v38, -1
	v_mov_b32_e32 v40, -1
	v_mov_b32_e32 v42, -1
	v_mov_b32_e32 v44, -1
	v_mov_b32_e32 v46, -1
	v_mov_b32_e32 v48, -1
	v_mov_b32_e32 v50, -1
	v_mov_b32_e32 v52, -1
	v_mov_b32_e32 v54, -1
	v_mov_b32_e32 v56, -1
	v_mov_b32_e32 v58, -1
	s_cmpk_lt_i32 s33, 0x1
	s_cbranch_scc1 .Lcsr_ld_done
	v_mov_b32_e32 v4, v0
	v_add_u32_e32 v5, 0x100, v0
	v_add_u32_e32 v6, 0x200, v0
	v_add_u32_e32 v7, 0x300, v0
	ds_read_b32 v12, v27 offset:34304
	v_mov_b32_e32 v16, 0x200
	s_waitcnt lgkmcnt(0)
	v_cmp_ge_i32_e64 s[20:21], v4, v12
	v_cmp_ge_i32_e64 s[22:23], v5, v12
	v_cmp_ge_i32_e64 s[24:25], v6, v12
	v_cmp_ge_i32_e64 s[26:27], v7, v12
	v_cndmask_b32_e64 v8, 0, v16, s[20:21]
	v_cndmask_b32_e64 v9, 0, v16, s[22:23]
	v_cndmask_b32_e64 v10, 0, v16, s[24:25]
	v_cndmask_b32_e64 v11, 0, v16, s[26:27]
	ds_read_b32 v12, v8 offset:34048
	ds_read_b32 v13, v9 offset:34048
	ds_read_b32 v14, v10 offset:34048
	ds_read_b32 v15, v11 offset:34048
	v_add_u32_e32 v16, 256, v8
	v_add_u32_e32 v17, 256, v9
	v_add_u32_e32 v18, 256, v10
	v_add_u32_e32 v19, 256, v11
	s_waitcnt lgkmcnt(3)
	v_cmp_ge_i32_e64 s[20:21], v4, v12
	s_waitcnt lgkmcnt(2)
	v_cmp_ge_i32_e64 s[22:23], v5, v13
	s_waitcnt lgkmcnt(1)
	v_cmp_ge_i32_e64 s[24:25], v6, v14
	s_waitcnt lgkmcnt(0)
	v_cmp_ge_i32_e64 s[26:27], v7, v15
	v_cndmask_b32_e64 v8, v8, v16, s[20:21]
	v_cndmask_b32_e64 v9, v9, v17, s[22:23]
	v_cndmask_b32_e64 v10, v10, v18, s[24:25]
	v_cndmask_b32_e64 v11, v11, v19, s[26:27]
	ds_read_b32 v12, v8 offset:33920
	ds_read_b32 v13, v9 offset:33920
	ds_read_b32 v14, v10 offset:33920
	ds_read_b32 v15, v11 offset:33920
	v_add_u32_e32 v16, 128, v8
	v_add_u32_e32 v17, 128, v9
	v_add_u32_e32 v18, 128, v10
	v_add_u32_e32 v19, 128, v11
	s_waitcnt lgkmcnt(3)
	v_cmp_ge_i32_e64 s[20:21], v4, v12
	s_waitcnt lgkmcnt(2)
	v_cmp_ge_i32_e64 s[22:23], v5, v13
	s_waitcnt lgkmcnt(1)
	v_cmp_ge_i32_e64 s[24:25], v6, v14
	s_waitcnt lgkmcnt(0)
	v_cmp_ge_i32_e64 s[26:27], v7, v15
	v_cndmask_b32_e64 v8, v8, v16, s[20:21]
	v_cndmask_b32_e64 v9, v9, v17, s[22:23]
	v_cndmask_b32_e64 v10, v10, v18, s[24:25]
	v_cndmask_b32_e64 v11, v11, v19, s[26:27]
	ds_read_b32 v12, v8 offset:33856
	ds_read_b32 v13, v9 offset:33856
	ds_read_b32 v14, v10 offset:33856
	ds_read_b32 v15, v11 offset:33856
	v_add_u32_e32 v16, 64, v8
	v_add_u32_e32 v17, 64, v9
	v_add_u32_e32 v18, 64, v10
	v_add_u32_e32 v19, 64, v11
	s_waitcnt lgkmcnt(3)
	v_cmp_ge_i32_e64 s[20:21], v4, v12
	s_waitcnt lgkmcnt(2)
	v_cmp_ge_i32_e64 s[22:23], v5, v13
	s_waitcnt lgkmcnt(1)
	v_cmp_ge_i32_e64 s[24:25], v6, v14
	s_waitcnt lgkmcnt(0)
	v_cmp_ge_i32_e64 s[26:27], v7, v15
	v_cndmask_b32_e64 v8, v8, v16, s[20:21]
	v_cndmask_b32_e64 v9, v9, v17, s[22:23]
	v_cndmask_b32_e64 v10, v10, v18, s[24:25]
	v_cndmask_b32_e64 v11, v11, v19, s[26:27]
	ds_read_b32 v12, v8 offset:33824
	ds_read_b32 v13, v9 offset:33824
	ds_read_b32 v14, v10 offset:33824
	ds_read_b32 v15, v11 offset:33824
	v_add_u32_e32 v16, 32, v8
	v_add_u32_e32 v17, 32, v9
	v_add_u32_e32 v18, 32, v10
	v_add_u32_e32 v19, 32, v11
	s_waitcnt lgkmcnt(3)
	v_cmp_ge_i32_e64 s[20:21], v4, v12
	s_waitcnt lgkmcnt(2)
	v_cmp_ge_i32_e64 s[22:23], v5, v13
	s_waitcnt lgkmcnt(1)
	v_cmp_ge_i32_e64 s[24:25], v6, v14
	s_waitcnt lgkmcnt(0)
	v_cmp_ge_i32_e64 s[26:27], v7, v15
	v_cndmask_b32_e64 v8, v8, v16, s[20:21]
	v_cndmask_b32_e64 v9, v9, v17, s[22:23]
	v_cndmask_b32_e64 v10, v10, v18, s[24:25]
	v_cndmask_b32_e64 v11, v11, v19, s[26:27]
	ds_read_b32 v12, v8 offset:33808
	ds_read_b32 v13, v9 offset:33808
	ds_read_b32 v14, v10 offset:33808
	ds_read_b32 v15, v11 offset:33808
	v_add_u32_e32 v16, 16, v8
	v_add_u32_e32 v17, 16, v9
	v_add_u32_e32 v18, 16, v10
	v_add_u32_e32 v19, 16, v11
	s_waitcnt lgkmcnt(3)
	v_cmp_ge_i32_e64 s[20:21], v4, v12
	s_waitcnt lgkmcnt(2)
	v_cmp_ge_i32_e64 s[22:23], v5, v13
	s_waitcnt lgkmcnt(1)
	v_cmp_ge_i32_e64 s[24:25], v6, v14
	s_waitcnt lgkmcnt(0)
	v_cmp_ge_i32_e64 s[26:27], v7, v15
	v_cndmask_b32_e64 v8, v8, v16, s[20:21]
	v_cndmask_b32_e64 v9, v9, v17, s[22:23]
	v_cndmask_b32_e64 v10, v10, v18, s[24:25]
	v_cndmask_b32_e64 v11, v11, v19, s[26:27]
	ds_read_b32 v12, v8 offset:33800
	ds_read_b32 v13, v9 offset:33800
	ds_read_b32 v14, v10 offset:33800
	ds_read_b32 v15, v11 offset:33800
	v_add_u32_e32 v16, 8, v8
	v_add_u32_e32 v17, 8, v9
	v_add_u32_e32 v18, 8, v10
	v_add_u32_e32 v19, 8, v11
	s_waitcnt lgkmcnt(3)
	v_cmp_ge_i32_e64 s[20:21], v4, v12
	s_waitcnt lgkmcnt(2)
	v_cmp_ge_i32_e64 s[22:23], v5, v13
	s_waitcnt lgkmcnt(1)
	v_cmp_ge_i32_e64 s[24:25], v6, v14
	s_waitcnt lgkmcnt(0)
	v_cmp_ge_i32_e64 s[26:27], v7, v15
	v_cndmask_b32_e64 v8, v8, v16, s[20:21]
	v_cndmask_b32_e64 v9, v9, v17, s[22:23]
	v_cndmask_b32_e64 v10, v10, v18, s[24:25]
	v_cndmask_b32_e64 v11, v11, v19, s[26:27]
	ds_read_b32 v12, v8 offset:33796
	ds_read_b32 v13, v9 offset:33796
	ds_read_b32 v14, v10 offset:33796
	ds_read_b32 v15, v11 offset:33796
	v_add_u32_e32 v16, 4, v8
	v_add_u32_e32 v17, 4, v9
	v_add_u32_e32 v18, 4, v10
	v_add_u32_e32 v19, 4, v11
	s_waitcnt lgkmcnt(3)
	v_cmp_ge_i32_e64 s[20:21], v4, v12
	s_waitcnt lgkmcnt(2)
	v_cmp_ge_i32_e64 s[22:23], v5, v13
	s_waitcnt lgkmcnt(1)
	v_cmp_ge_i32_e64 s[24:25], v6, v14
	s_waitcnt lgkmcnt(0)
	v_cmp_ge_i32_e64 s[26:27], v7, v15
	v_cndmask_b32_e64 v8, v8, v16, s[20:21]
	v_cndmask_b32_e64 v9, v9, v17, s[22:23]
	v_cndmask_b32_e64 v10, v10, v18, s[24:25]
	v_cndmask_b32_e64 v11, v11, v19, s[26:27]
	ds_read2st64_b32 v[12:13], v8 offset0:132 offset1:140
	ds_read2st64_b32 v[14:15], v9 offset0:132 offset1:140
	ds_read2st64_b32 v[16:17], v10 offset0:132 offset1:140
	ds_read2st64_b32 v[18:19], v11 offset0:132 offset1:140
	v_cmp_gt_i32_e64 s[20:21], s33, v4
	v_cmp_gt_i32_e64 s[22:23], s33, v5
	v_cmp_gt_i32_e64 s[24:25], s33, v6
	v_cmp_gt_i32_e64 s[26:27], s33, v7
	s_waitcnt lgkmcnt(3)
	v_sub_u32_e32 v12, v13, v12
	v_add_u32_e32 v12, v12, v4
	v_mov_b32_e32 v13, 0
	v_lshl_add_u64 v[12:13], v[12:13], 3, s[52:53]
	s_waitcnt lgkmcnt(2)
	v_sub_u32_e32 v14, v15, v14
	v_add_u32_e32 v14, v14, v5
	v_mov_b32_e32 v15, 0
	v_lshl_add_u64 v[14:15], v[14:15], 3, s[52:53]
	s_waitcnt lgkmcnt(1)
	v_sub_u32_e32 v16, v17, v16
	v_add_u32_e32 v16, v16, v6
	v_mov_b32_e32 v17, 0
	v_lshl_add_u64 v[16:17], v[16:17], 3, s[52:53]
	s_waitcnt lgkmcnt(0)
	v_sub_u32_e32 v18, v19, v18
	v_add_u32_e32 v18, v18, v7
	v_mov_b32_e32 v19, 0
	v_lshl_add_u64 v[18:19], v[18:19], 3, s[52:53]
	s_mov_b64 exec, s[20:21]
	s_cbranch_execz .Lcsr_ld_skip0
	global_load_dwordx2 v[28:29], v[12:13], off
.Lcsr_ld_skip0:
	s_mov_b64 exec, s[22:23]
	s_cbranch_execz .Lcsr_ld_skip1
	global_load_dwordx2 v[30:31], v[14:15], off
.Lcsr_ld_skip1:
	s_mov_b64 exec, s[24:25]
	s_cbranch_execz .Lcsr_ld_skip2
	global_load_dwordx2 v[32:33], v[16:17], off
.Lcsr_ld_skip2:
	s_mov_b64 exec, s[26:27]
	s_cbranch_execz .Lcsr_ld_skip3
	global_load_dwordx2 v[34:35], v[18:19], off
.Lcsr_ld_skip3:
	s_mov_b64 exec, -1
	s_cmpk_lt_i32 s33, 0x401
	s_cbranch_scc1 .Lcsr_ld_done
	v_add_u32_e32 v4, 0x400, v0
	v_add_u32_e32 v5, 0x500, v0
	v_add_u32_e32 v6, 0x600, v0
	v_add_u32_e32 v7, 0x700, v0
	ds_read_b32 v12, v27 offset:34304
	v_mov_b32_e32 v16, 0x200
	s_waitcnt lgkmcnt(0)
	v_cmp_ge_i32_e64 s[20:21], v4, v12
	v_cmp_ge_i32_e64 s[22:23], v5, v12
	v_cmp_ge_i32_e64 s[24:25], v6, v12
	v_cmp_ge_i32_e64 s[26:27], v7, v12
	v_cndmask_b32_e64 v8, 0, v16, s[20:21]
	v_cndmask_b32_e64 v9, 0, v16, s[22:23]
	v_cndmask_b32_e64 v10, 0, v16, s[24:25]
	v_cndmask_b32_e64 v11, 0, v16, s[26:27]
	ds_read_b32 v12, v8 offset:34048
	ds_read_b32 v13, v9 offset:34048
	ds_read_b32 v14, v10 offset:34048
	ds_read_b32 v15, v11 offset:34048
	v_add_u32_e32 v16, 256, v8
	v_add_u32_e32 v17, 256, v9
	v_add_u32_e32 v18, 256, v10
	v_add_u32_e32 v19, 256, v11
	s_waitcnt lgkmcnt(3)
	v_cmp_ge_i32_e64 s[20:21], v4, v12
	s_waitcnt lgkmcnt(2)
	v_cmp_ge_i32_e64 s[22:23], v5, v13
	s_waitcnt lgkmcnt(1)
	v_cmp_ge_i32_e64 s[24:25], v6, v14
	s_waitcnt lgkmcnt(0)
	v_cmp_ge_i32_e64 s[26:27], v7, v15
	v_cndmask_b32_e64 v8, v8, v16, s[20:21]
	v_cndmask_b32_e64 v9, v9, v17, s[22:23]
	v_cndmask_b32_e64 v10, v10, v18, s[24:25]
	v_cndmask_b32_e64 v11, v11, v19, s[26:27]
	ds_read_b32 v12, v8 offset:33920
	ds_read_b32 v13, v9 offset:33920
	ds_read_b32 v14, v10 offset:33920
	ds_read_b32 v15, v11 offset:33920
	v_add_u32_e32 v16, 128, v8
	v_add_u32_e32 v17, 128, v9
	v_add_u32_e32 v18, 128, v10
	v_add_u32_e32 v19, 128, v11
	s_waitcnt lgkmcnt(3)
	v_cmp_ge_i32_e64 s[20:21], v4, v12
	s_waitcnt lgkmcnt(2)
	v_cmp_ge_i32_e64 s[22:23], v5, v13
	s_waitcnt lgkmcnt(1)
	v_cmp_ge_i32_e64 s[24:25], v6, v14
	s_waitcnt lgkmcnt(0)
	v_cmp_ge_i32_e64 s[26:27], v7, v15
	v_cndmask_b32_e64 v8, v8, v16, s[20:21]
	v_cndmask_b32_e64 v9, v9, v17, s[22:23]
	v_cndmask_b32_e64 v10, v10, v18, s[24:25]
	v_cndmask_b32_e64 v11, v11, v19, s[26:27]
	ds_read_b32 v12, v8 offset:33856
	ds_read_b32 v13, v9 offset:33856
	ds_read_b32 v14, v10 offset:33856
	ds_read_b32 v15, v11 offset:33856
	v_add_u32_e32 v16, 64, v8
	v_add_u32_e32 v17, 64, v9
	v_add_u32_e32 v18, 64, v10
	v_add_u32_e32 v19, 64, v11
	s_waitcnt lgkmcnt(3)
	v_cmp_ge_i32_e64 s[20:21], v4, v12
	s_waitcnt lgkmcnt(2)
	v_cmp_ge_i32_e64 s[22:23], v5, v13
	s_waitcnt lgkmcnt(1)
	v_cmp_ge_i32_e64 s[24:25], v6, v14
	s_waitcnt lgkmcnt(0)
	v_cmp_ge_i32_e64 s[26:27], v7, v15
	v_cndmask_b32_e64 v8, v8, v16, s[20:21]
	v_cndmask_b32_e64 v9, v9, v17, s[22:23]
	v_cndmask_b32_e64 v10, v10, v18, s[24:25]
	v_cndmask_b32_e64 v11, v11, v19, s[26:27]
	ds_read_b32 v12, v8 offset:33824
	ds_read_b32 v13, v9 offset:33824
	ds_read_b32 v14, v10 offset:33824
	ds_read_b32 v15, v11 offset:33824
	v_add_u32_e32 v16, 32, v8
	v_add_u32_e32 v17, 32, v9
	v_add_u32_e32 v18, 32, v10
	v_add_u32_e32 v19, 32, v11
	s_waitcnt lgkmcnt(3)
	v_cmp_ge_i32_e64 s[20:21], v4, v12
	s_waitcnt lgkmcnt(2)
	v_cmp_ge_i32_e64 s[22:23], v5, v13
	s_waitcnt lgkmcnt(1)
	v_cmp_ge_i32_e64 s[24:25], v6, v14
	s_waitcnt lgkmcnt(0)
	v_cmp_ge_i32_e64 s[26:27], v7, v15
	v_cndmask_b32_e64 v8, v8, v16, s[20:21]
	v_cndmask_b32_e64 v9, v9, v17, s[22:23]
	v_cndmask_b32_e64 v10, v10, v18, s[24:25]
	v_cndmask_b32_e64 v11, v11, v19, s[26:27]
	ds_read_b32 v12, v8 offset:33808
	ds_read_b32 v13, v9 offset:33808
	ds_read_b32 v14, v10 offset:33808
	ds_read_b32 v15, v11 offset:33808
	v_add_u32_e32 v16, 16, v8
	v_add_u32_e32 v17, 16, v9
	v_add_u32_e32 v18, 16, v10
	v_add_u32_e32 v19, 16, v11
	s_waitcnt lgkmcnt(3)
	v_cmp_ge_i32_e64 s[20:21], v4, v12
	s_waitcnt lgkmcnt(2)
	v_cmp_ge_i32_e64 s[22:23], v5, v13
	s_waitcnt lgkmcnt(1)
	v_cmp_ge_i32_e64 s[24:25], v6, v14
	s_waitcnt lgkmcnt(0)
	v_cmp_ge_i32_e64 s[26:27], v7, v15
	v_cndmask_b32_e64 v8, v8, v16, s[20:21]
	v_cndmask_b32_e64 v9, v9, v17, s[22:23]
	v_cndmask_b32_e64 v10, v10, v18, s[24:25]
	v_cndmask_b32_e64 v11, v11, v19, s[26:27]
	ds_read_b32 v12, v8 offset:33800
	ds_read_b32 v13, v9 offset:33800
	ds_read_b32 v14, v10 offset:33800
	ds_read_b32 v15, v11 offset:33800
	v_add_u32_e32 v16, 8, v8
	v_add_u32_e32 v17, 8, v9
	v_add_u32_e32 v18, 8, v10
	v_add_u32_e32 v19, 8, v11
	s_waitcnt lgkmcnt(3)
	v_cmp_ge_i32_e64 s[20:21], v4, v12
	s_waitcnt lgkmcnt(2)
	v_cmp_ge_i32_e64 s[22:23], v5, v13
	s_waitcnt lgkmcnt(1)
	v_cmp_ge_i32_e64 s[24:25], v6, v14
	s_waitcnt lgkmcnt(0)
	v_cmp_ge_i32_e64 s[26:27], v7, v15
	v_cndmask_b32_e64 v8, v8, v16, s[20:21]
	v_cndmask_b32_e64 v9, v9, v17, s[22:23]
	v_cndmask_b32_e64 v10, v10, v18, s[24:25]
	v_cndmask_b32_e64 v11, v11, v19, s[26:27]
	ds_read_b32 v12, v8 offset:33796
	ds_read_b32 v13, v9 offset:33796
	ds_read_b32 v14, v10 offset:33796
	ds_read_b32 v15, v11 offset:33796
	v_add_u32_e32 v16, 4, v8
	v_add_u32_e32 v17, 4, v9
	v_add_u32_e32 v18, 4, v10
	v_add_u32_e32 v19, 4, v11
	s_waitcnt lgkmcnt(3)
	v_cmp_ge_i32_e64 s[20:21], v4, v12
	s_waitcnt lgkmcnt(2)
	v_cmp_ge_i32_e64 s[22:23], v5, v13
	s_waitcnt lgkmcnt(1)
	v_cmp_ge_i32_e64 s[24:25], v6, v14
	s_waitcnt lgkmcnt(0)
	v_cmp_ge_i32_e64 s[26:27], v7, v15
	v_cndmask_b32_e64 v8, v8, v16, s[20:21]
	v_cndmask_b32_e64 v9, v9, v17, s[22:23]
	v_cndmask_b32_e64 v10, v10, v18, s[24:25]
	v_cndmask_b32_e64 v11, v11, v19, s[26:27]
	ds_read2st64_b32 v[12:13], v8 offset0:132 offset1:140
	ds_read2st64_b32 v[14:15], v9 offset0:132 offset1:140
	ds_read2st64_b32 v[16:17], v10 offset0:132 offset1:140
	ds_read2st64_b32 v[18:19], v11 offset0:132 offset1:140
	v_cmp_gt_i32_e64 s[20:21], s33, v4
	v_cmp_gt_i32_e64 s[22:23], s33, v5
	v_cmp_gt_i32_e64 s[24:25], s33, v6
	v_cmp_gt_i32_e64 s[26:27], s33, v7
	s_waitcnt lgkmcnt(3)
	v_sub_u32_e32 v12, v13, v12
	v_add_u32_e32 v12, v12, v4
	v_mov_b32_e32 v13, 0
	v_lshl_add_u64 v[12:13], v[12:13], 3, s[52:53]
	s_waitcnt lgkmcnt(2)
	v_sub_u32_e32 v14, v15, v14
	v_add_u32_e32 v14, v14, v5
	v_mov_b32_e32 v15, 0
	v_lshl_add_u64 v[14:15], v[14:15], 3, s[52:53]
	s_waitcnt lgkmcnt(1)
	v_sub_u32_e32 v16, v17, v16
	v_add_u32_e32 v16, v16, v6
	v_mov_b32_e32 v17, 0
	v_lshl_add_u64 v[16:17], v[16:17], 3, s[52:53]
	s_waitcnt lgkmcnt(0)
	v_sub_u32_e32 v18, v19, v18
	v_add_u32_e32 v18, v18, v7
	v_mov_b32_e32 v19, 0
	v_lshl_add_u64 v[18:19], v[18:19], 3, s[52:53]
	s_mov_b64 exec, s[20:21]
	s_cbranch_execz .Lcsr_ld_skip4
	global_load_dwordx2 v[36:37], v[12:13], off
.Lcsr_ld_skip4:
	s_mov_b64 exec, s[22:23]
	s_cbranch_execz .Lcsr_ld_skip5
	global_load_dwordx2 v[38:39], v[14:15], off
.Lcsr_ld_skip5:
	s_mov_b64 exec, s[24:25]
	s_cbranch_execz .Lcsr_ld_skip6
	global_load_dwordx2 v[40:41], v[16:17], off
.Lcsr_ld_skip6:
	s_mov_b64 exec, s[26:27]
	s_cbranch_execz .Lcsr_ld_skip7
	global_load_dwordx2 v[42:43], v[18:19], off
.Lcsr_ld_skip7:
	s_mov_b64 exec, -1
	s_cmpk_lt_i32 s33, 0x801
	s_cbranch_scc1 .Lcsr_ld_done
	v_add_u32_e32 v4, 0x800, v0
	v_add_u32_e32 v5, 0x900, v0
	v_add_u32_e32 v6, 0xa00, v0
	v_add_u32_e32 v7, 0xb00, v0
	ds_read_b32 v12, v27 offset:34304
	v_mov_b32_e32 v16, 0x200
	s_waitcnt lgkmcnt(0)
	v_cmp_ge_i32_e64 s[20:21], v4, v12
	v_cmp_ge_i32_e64 s[22:23], v5, v12
	v_cmp_ge_i32_e64 s[24:25], v6, v12
	v_cmp_ge_i32_e64 s[26:27], v7, v12
	v_cndmask_b32_e64 v8, 0, v16, s[20:21]
	v_cndmask_b32_e64 v9, 0, v16, s[22:23]
	v_cndmask_b32_e64 v10, 0, v16, s[24:25]
	v_cndmask_b32_e64 v11, 0, v16, s[26:27]
	ds_read_b32 v12, v8 offset:34048
	ds_read_b32 v13, v9 offset:34048
	ds_read_b32 v14, v10 offset:34048
	ds_read_b32 v15, v11 offset:34048
	v_add_u32_e32 v16, 256, v8
	v_add_u32_e32 v17, 256, v9
	v_add_u32_e32 v18, 256, v10
	v_add_u32_e32 v19, 256, v11
	s_waitcnt lgkmcnt(3)
	v_cmp_ge_i32_e64 s[20:21], v4, v12
	s_waitcnt lgkmcnt(2)
	v_cmp_ge_i32_e64 s[22:23], v5, v13
	s_waitcnt lgkmcnt(1)
	v_cmp_ge_i32_e64 s[24:25], v6, v14
	s_waitcnt lgkmcnt(0)
	v_cmp_ge_i32_e64 s[26:27], v7, v15
	v_cndmask_b32_e64 v8, v8, v16, s[20:21]
	v_cndmask_b32_e64 v9, v9, v17, s[22:23]
	v_cndmask_b32_e64 v10, v10, v18, s[24:25]
	v_cndmask_b32_e64 v11, v11, v19, s[26:27]
	ds_read_b32 v12, v8 offset:33920
	ds_read_b32 v13, v9 offset:33920
	ds_read_b32 v14, v10 offset:33920
	ds_read_b32 v15, v11 offset:33920
	v_add_u32_e32 v16, 128, v8
	v_add_u32_e32 v17, 128, v9
	v_add_u32_e32 v18, 128, v10
	v_add_u32_e32 v19, 128, v11
	s_waitcnt lgkmcnt(3)
	v_cmp_ge_i32_e64 s[20:21], v4, v12
	s_waitcnt lgkmcnt(2)
	v_cmp_ge_i32_e64 s[22:23], v5, v13
	s_waitcnt lgkmcnt(1)
	v_cmp_ge_i32_e64 s[24:25], v6, v14
	s_waitcnt lgkmcnt(0)
	v_cmp_ge_i32_e64 s[26:27], v7, v15
	v_cndmask_b32_e64 v8, v8, v16, s[20:21]
	v_cndmask_b32_e64 v9, v9, v17, s[22:23]
	v_cndmask_b32_e64 v10, v10, v18, s[24:25]
	v_cndmask_b32_e64 v11, v11, v19, s[26:27]
	ds_read_b32 v12, v8 offset:33856
	ds_read_b32 v13, v9 offset:33856
	ds_read_b32 v14, v10 offset:33856
	ds_read_b32 v15, v11 offset:33856
	v_add_u32_e32 v16, 64, v8
	v_add_u32_e32 v17, 64, v9
	v_add_u32_e32 v18, 64, v10
	v_add_u32_e32 v19, 64, v11
	s_waitcnt lgkmcnt(3)
	v_cmp_ge_i32_e64 s[20:21], v4, v12
	s_waitcnt lgkmcnt(2)
	v_cmp_ge_i32_e64 s[22:23], v5, v13
	s_waitcnt lgkmcnt(1)
	v_cmp_ge_i32_e64 s[24:25], v6, v14
	s_waitcnt lgkmcnt(0)
	v_cmp_ge_i32_e64 s[26:27], v7, v15
	v_cndmask_b32_e64 v8, v8, v16, s[20:21]
	v_cndmask_b32_e64 v9, v9, v17, s[22:23]
	v_cndmask_b32_e64 v10, v10, v18, s[24:25]
	v_cndmask_b32_e64 v11, v11, v19, s[26:27]
	ds_read_b32 v12, v8 offset:33824
	ds_read_b32 v13, v9 offset:33824
	ds_read_b32 v14, v10 offset:33824
	ds_read_b32 v15, v11 offset:33824
	v_add_u32_e32 v16, 32, v8
	v_add_u32_e32 v17, 32, v9
	v_add_u32_e32 v18, 32, v10
	v_add_u32_e32 v19, 32, v11
	s_waitcnt lgkmcnt(3)
	v_cmp_ge_i32_e64 s[20:21], v4, v12
	s_waitcnt lgkmcnt(2)
	v_cmp_ge_i32_e64 s[22:23], v5, v13
	s_waitcnt lgkmcnt(1)
	v_cmp_ge_i32_e64 s[24:25], v6, v14
	s_waitcnt lgkmcnt(0)
	v_cmp_ge_i32_e64 s[26:27], v7, v15
	v_cndmask_b32_e64 v8, v8, v16, s[20:21]
	v_cndmask_b32_e64 v9, v9, v17, s[22:23]
	v_cndmask_b32_e64 v10, v10, v18, s[24:25]
	v_cndmask_b32_e64 v11, v11, v19, s[26:27]
	ds_read_b32 v12, v8 offset:33808
	ds_read_b32 v13, v9 offset:33808
	ds_read_b32 v14, v10 offset:33808
	ds_read_b32 v15, v11 offset:33808
	v_add_u32_e32 v16, 16, v8
	v_add_u32_e32 v17, 16, v9
	v_add_u32_e32 v18, 16, v10
	v_add_u32_e32 v19, 16, v11
	s_waitcnt lgkmcnt(3)
	v_cmp_ge_i32_e64 s[20:21], v4, v12
	s_waitcnt lgkmcnt(2)
	v_cmp_ge_i32_e64 s[22:23], v5, v13
	s_waitcnt lgkmcnt(1)
	v_cmp_ge_i32_e64 s[24:25], v6, v14
	s_waitcnt lgkmcnt(0)
	v_cmp_ge_i32_e64 s[26:27], v7, v15
	v_cndmask_b32_e64 v8, v8, v16, s[20:21]
	v_cndmask_b32_e64 v9, v9, v17, s[22:23]
	v_cndmask_b32_e64 v10, v10, v18, s[24:25]
	v_cndmask_b32_e64 v11, v11, v19, s[26:27]
	ds_read_b32 v12, v8 offset:33800
	ds_read_b32 v13, v9 offset:33800
	ds_read_b32 v14, v10 offset:33800
	ds_read_b32 v15, v11 offset:33800
	v_add_u32_e32 v16, 8, v8
	v_add_u32_e32 v17, 8, v9
	v_add_u32_e32 v18, 8, v10
	v_add_u32_e32 v19, 8, v11
	s_waitcnt lgkmcnt(3)
	v_cmp_ge_i32_e64 s[20:21], v4, v12
	s_waitcnt lgkmcnt(2)
	v_cmp_ge_i32_e64 s[22:23], v5, v13
	s_waitcnt lgkmcnt(1)
	v_cmp_ge_i32_e64 s[24:25], v6, v14
	s_waitcnt lgkmcnt(0)
	v_cmp_ge_i32_e64 s[26:27], v7, v15
	v_cndmask_b32_e64 v8, v8, v16, s[20:21]
	v_cndmask_b32_e64 v9, v9, v17, s[22:23]
	v_cndmask_b32_e64 v10, v10, v18, s[24:25]
	v_cndmask_b32_e64 v11, v11, v19, s[26:27]
	ds_read_b32 v12, v8 offset:33796
	ds_read_b32 v13, v9 offset:33796
	ds_read_b32 v14, v10 offset:33796
	ds_read_b32 v15, v11 offset:33796
	v_add_u32_e32 v16, 4, v8
	v_add_u32_e32 v17, 4, v9
	v_add_u32_e32 v18, 4, v10
	v_add_u32_e32 v19, 4, v11
	s_waitcnt lgkmcnt(3)
	v_cmp_ge_i32_e64 s[20:21], v4, v12
	s_waitcnt lgkmcnt(2)
	v_cmp_ge_i32_e64 s[22:23], v5, v13
	s_waitcnt lgkmcnt(1)
	v_cmp_ge_i32_e64 s[24:25], v6, v14
	s_waitcnt lgkmcnt(0)
	v_cmp_ge_i32_e64 s[26:27], v7, v15
	v_cndmask_b32_e64 v8, v8, v16, s[20:21]
	v_cndmask_b32_e64 v9, v9, v17, s[22:23]
	v_cndmask_b32_e64 v10, v10, v18, s[24:25]
	v_cndmask_b32_e64 v11, v11, v19, s[26:27]
	ds_read2st64_b32 v[12:13], v8 offset0:132 offset1:140
	ds_read2st64_b32 v[14:15], v9 offset0:132 offset1:140
	ds_read2st64_b32 v[16:17], v10 offset0:132 offset1:140
	ds_read2st64_b32 v[18:19], v11 offset0:132 offset1:140
	v_cmp_gt_i32_e64 s[20:21], s33, v4
	v_cmp_gt_i32_e64 s[22:23], s33, v5
	v_cmp_gt_i32_e64 s[24:25], s33, v6
	v_cmp_gt_i32_e64 s[26:27], s33, v7
	s_waitcnt lgkmcnt(3)
	v_sub_u32_e32 v12, v13, v12
	v_add_u32_e32 v12, v12, v4
	v_mov_b32_e32 v13, 0
	v_lshl_add_u64 v[12:13], v[12:13], 3, s[52:53]
	s_waitcnt lgkmcnt(2)
	v_sub_u32_e32 v14, v15, v14
	v_add_u32_e32 v14, v14, v5
	v_mov_b32_e32 v15, 0
	v_lshl_add_u64 v[14:15], v[14:15], 3, s[52:53]
	s_waitcnt lgkmcnt(1)
	v_sub_u32_e32 v16, v17, v16
	v_add_u32_e32 v16, v16, v6
	v_mov_b32_e32 v17, 0
	v_lshl_add_u64 v[16:17], v[16:17], 3, s[52:53]
	s_waitcnt lgkmcnt(0)
	v_sub_u32_e32 v18, v19, v18
	v_add_u32_e32 v18, v18, v7
	v_mov_b32_e32 v19, 0
	v_lshl_add_u64 v[18:19], v[18:19], 3, s[52:53]
	s_mov_b64 exec, s[20:21]
	s_cbranch_execz .Lcsr_ld_skip8
	global_load_dwordx2 v[44:45], v[12:13], off
.Lcsr_ld_skip8:
	s_mov_b64 exec, s[22:23]
	s_cbranch_execz .Lcsr_ld_skip9
	global_load_dwordx2 v[46:47], v[14:15], off
.Lcsr_ld_skip9:
	s_mov_b64 exec, s[24:25]
	s_cbranch_execz .Lcsr_ld_skip10
	global_load_dwordx2 v[48:49], v[16:17], off
.Lcsr_ld_skip10:
	s_mov_b64 exec, s[26:27]
	s_cbranch_execz .Lcsr_ld_skip11
	global_load_dwordx2 v[50:51], v[18:19], off
.Lcsr_ld_skip11:
	s_mov_b64 exec, -1
	s_cmpk_lt_i32 s33, 0xc01
	s_cbranch_scc1 .Lcsr_ld_done
	v_add_u32_e32 v4, 0xc00, v0
	v_add_u32_e32 v5, 0xd00, v0
	v_add_u32_e32 v6, 0xe00, v0
	v_add_u32_e32 v7, 0xf00, v0
	ds_read_b32 v12, v27 offset:34304
	v_mov_b32_e32 v16, 0x200
	s_waitcnt lgkmcnt(0)
	v_cmp_ge_i32_e64 s[20:21], v4, v12
	v_cmp_ge_i32_e64 s[22:23], v5, v12
	v_cmp_ge_i32_e64 s[24:25], v6, v12
	v_cmp_ge_i32_e64 s[26:27], v7, v12
	v_cndmask_b32_e64 v8, 0, v16, s[20:21]
	v_cndmask_b32_e64 v9, 0, v16, s[22:23]
	v_cndmask_b32_e64 v10, 0, v16, s[24:25]
	v_cndmask_b32_e64 v11, 0, v16, s[26:27]
	ds_read_b32 v12, v8 offset:34048
	ds_read_b32 v13, v9 offset:34048
	ds_read_b32 v14, v10 offset:34048
	ds_read_b32 v15, v11 offset:34048
	v_add_u32_e32 v16, 256, v8
	v_add_u32_e32 v17, 256, v9
	v_add_u32_e32 v18, 256, v10
	v_add_u32_e32 v19, 256, v11
	s_waitcnt lgkmcnt(3)
	v_cmp_ge_i32_e64 s[20:21], v4, v12
	s_waitcnt lgkmcnt(2)
	v_cmp_ge_i32_e64 s[22:23], v5, v13
	s_waitcnt lgkmcnt(1)
	v_cmp_ge_i32_e64 s[24:25], v6, v14
	s_waitcnt lgkmcnt(0)
	v_cmp_ge_i32_e64 s[26:27], v7, v15
	v_cndmask_b32_e64 v8, v8, v16, s[20:21]
	v_cndmask_b32_e64 v9, v9, v17, s[22:23]
	v_cndmask_b32_e64 v10, v10, v18, s[24:25]
	v_cndmask_b32_e64 v11, v11, v19, s[26:27]
	ds_read_b32 v12, v8 offset:33920
	ds_read_b32 v13, v9 offset:33920
	ds_read_b32 v14, v10 offset:33920
	ds_read_b32 v15, v11 offset:33920
	v_add_u32_e32 v16, 128, v8
	v_add_u32_e32 v17, 128, v9
	v_add_u32_e32 v18, 128, v10
	v_add_u32_e32 v19, 128, v11
	s_waitcnt lgkmcnt(3)
	v_cmp_ge_i32_e64 s[20:21], v4, v12
	s_waitcnt lgkmcnt(2)
	v_cmp_ge_i32_e64 s[22:23], v5, v13
	s_waitcnt lgkmcnt(1)
	v_cmp_ge_i32_e64 s[24:25], v6, v14
	s_waitcnt lgkmcnt(0)
	v_cmp_ge_i32_e64 s[26:27], v7, v15
	v_cndmask_b32_e64 v8, v8, v16, s[20:21]
	v_cndmask_b32_e64 v9, v9, v17, s[22:23]
	v_cndmask_b32_e64 v10, v10, v18, s[24:25]
	v_cndmask_b32_e64 v11, v11, v19, s[26:27]
	ds_read_b32 v12, v8 offset:33856
	ds_read_b32 v13, v9 offset:33856
	ds_read_b32 v14, v10 offset:33856
	ds_read_b32 v15, v11 offset:33856
	v_add_u32_e32 v16, 64, v8
	v_add_u32_e32 v17, 64, v9
	v_add_u32_e32 v18, 64, v10
	v_add_u32_e32 v19, 64, v11
	s_waitcnt lgkmcnt(3)
	v_cmp_ge_i32_e64 s[20:21], v4, v12
	s_waitcnt lgkmcnt(2)
	v_cmp_ge_i32_e64 s[22:23], v5, v13
	s_waitcnt lgkmcnt(1)
	v_cmp_ge_i32_e64 s[24:25], v6, v14
	s_waitcnt lgkmcnt(0)
	v_cmp_ge_i32_e64 s[26:27], v7, v15
	v_cndmask_b32_e64 v8, v8, v16, s[20:21]
	v_cndmask_b32_e64 v9, v9, v17, s[22:23]
	v_cndmask_b32_e64 v10, v10, v18, s[24:25]
	v_cndmask_b32_e64 v11, v11, v19, s[26:27]
	ds_read_b32 v12, v8 offset:33824
	ds_read_b32 v13, v9 offset:33824
	ds_read_b32 v14, v10 offset:33824
	ds_read_b32 v15, v11 offset:33824
	v_add_u32_e32 v16, 32, v8
	v_add_u32_e32 v17, 32, v9
	v_add_u32_e32 v18, 32, v10
	v_add_u32_e32 v19, 32, v11
	s_waitcnt lgkmcnt(3)
	v_cmp_ge_i32_e64 s[20:21], v4, v12
	s_waitcnt lgkmcnt(2)
	v_cmp_ge_i32_e64 s[22:23], v5, v13
	s_waitcnt lgkmcnt(1)
	v_cmp_ge_i32_e64 s[24:25], v6, v14
	s_waitcnt lgkmcnt(0)
	v_cmp_ge_i32_e64 s[26:27], v7, v15
	v_cndmask_b32_e64 v8, v8, v16, s[20:21]
	v_cndmask_b32_e64 v9, v9, v17, s[22:23]
	v_cndmask_b32_e64 v10, v10, v18, s[24:25]
	v_cndmask_b32_e64 v11, v11, v19, s[26:27]
	ds_read_b32 v12, v8 offset:33808
	ds_read_b32 v13, v9 offset:33808
	ds_read_b32 v14, v10 offset:33808
	ds_read_b32 v15, v11 offset:33808
	v_add_u32_e32 v16, 16, v8
	v_add_u32_e32 v17, 16, v9
	v_add_u32_e32 v18, 16, v10
	v_add_u32_e32 v19, 16, v11
	s_waitcnt lgkmcnt(3)
	v_cmp_ge_i32_e64 s[20:21], v4, v12
	s_waitcnt lgkmcnt(2)
	v_cmp_ge_i32_e64 s[22:23], v5, v13
	s_waitcnt lgkmcnt(1)
	v_cmp_ge_i32_e64 s[24:25], v6, v14
	s_waitcnt lgkmcnt(0)
	v_cmp_ge_i32_e64 s[26:27], v7, v15
	v_cndmask_b32_e64 v8, v8, v16, s[20:21]
	v_cndmask_b32_e64 v9, v9, v17, s[22:23]
	v_cndmask_b32_e64 v10, v10, v18, s[24:25]
	v_cndmask_b32_e64 v11, v11, v19, s[26:27]
	ds_read_b32 v12, v8 offset:33800
	ds_read_b32 v13, v9 offset:33800
	ds_read_b32 v14, v10 offset:33800
	ds_read_b32 v15, v11 offset:33800
	v_add_u32_e32 v16, 8, v8
	v_add_u32_e32 v17, 8, v9
	v_add_u32_e32 v18, 8, v10
	v_add_u32_e32 v19, 8, v11
	s_waitcnt lgkmcnt(3)
	v_cmp_ge_i32_e64 s[20:21], v4, v12
	s_waitcnt lgkmcnt(2)
	v_cmp_ge_i32_e64 s[22:23], v5, v13
	s_waitcnt lgkmcnt(1)
	v_cmp_ge_i32_e64 s[24:25], v6, v14
	s_waitcnt lgkmcnt(0)
	v_cmp_ge_i32_e64 s[26:27], v7, v15
	v_cndmask_b32_e64 v8, v8, v16, s[20:21]
	v_cndmask_b32_e64 v9, v9, v17, s[22:23]
	v_cndmask_b32_e64 v10, v10, v18, s[24:25]
	v_cndmask_b32_e64 v11, v11, v19, s[26:27]
	ds_read_b32 v12, v8 offset:33796
	ds_read_b32 v13, v9 offset:33796
	ds_read_b32 v14, v10 offset:33796
	ds_read_b32 v15, v11 offset:33796
	v_add_u32_e32 v16, 4, v8
	v_add_u32_e32 v17, 4, v9
	v_add_u32_e32 v18, 4, v10
	v_add_u32_e32 v19, 4, v11
	s_waitcnt lgkmcnt(3)
	v_cmp_ge_i32_e64 s[20:21], v4, v12
	s_waitcnt lgkmcnt(2)
	v_cmp_ge_i32_e64 s[22:23], v5, v13
	s_waitcnt lgkmcnt(1)
	v_cmp_ge_i32_e64 s[24:25], v6, v14
	s_waitcnt lgkmcnt(0)
	v_cmp_ge_i32_e64 s[26:27], v7, v15
	v_cndmask_b32_e64 v8, v8, v16, s[20:21]
	v_cndmask_b32_e64 v9, v9, v17, s[22:23]
	v_cndmask_b32_e64 v10, v10, v18, s[24:25]
	v_cndmask_b32_e64 v11, v11, v19, s[26:27]
	ds_read2st64_b32 v[12:13], v8 offset0:132 offset1:140
	ds_read2st64_b32 v[14:15], v9 offset0:132 offset1:140
	ds_read2st64_b32 v[16:17], v10 offset0:132 offset1:140
	ds_read2st64_b32 v[18:19], v11 offset0:132 offset1:140
	v_cmp_gt_i32_e64 s[20:21], s33, v4
	v_cmp_gt_i32_e64 s[22:23], s33, v5
	v_cmp_gt_i32_e64 s[24:25], s33, v6
	v_cmp_gt_i32_e64 s[26:27], s33, v7
	s_waitcnt lgkmcnt(3)
	v_sub_u32_e32 v12, v13, v12
	v_add_u32_e32 v12, v12, v4
	v_mov_b32_e32 v13, 0
	v_lshl_add_u64 v[12:13], v[12:13], 3, s[52:53]
	s_waitcnt lgkmcnt(2)
	v_sub_u32_e32 v14, v15, v14
	v_add_u32_e32 v14, v14, v5
	v_mov_b32_e32 v15, 0
	v_lshl_add_u64 v[14:15], v[14:15], 3, s[52:53]
	s_waitcnt lgkmcnt(1)
	v_sub_u32_e32 v16, v17, v16
	v_add_u32_e32 v16, v16, v6
	v_mov_b32_e32 v17, 0
	v_lshl_add_u64 v[16:17], v[16:17], 3, s[52:53]
	s_waitcnt lgkmcnt(0)
	v_sub_u32_e32 v18, v19, v18
	v_add_u32_e32 v18, v18, v7
	v_mov_b32_e32 v19, 0
	v_lshl_add_u64 v[18:19], v[18:19], 3, s[52:53]
	s_mov_b64 exec, s[20:21]
	s_cbranch_execz .Lcsr_ld_skip12
	global_load_dwordx2 v[52:53], v[12:13], off
.Lcsr_ld_skip12:
	s_mov_b64 exec, s[22:23]
	s_cbranch_execz .Lcsr_ld_skip13
	global_load_dwordx2 v[54:55], v[14:15], off
.Lcsr_ld_skip13:
	s_mov_b64 exec, s[24:25]
	s_cbranch_execz .Lcsr_ld_skip14
	global_load_dwordx2 v[56:57], v[16:17], off
.Lcsr_ld_skip14:
	s_mov_b64 exec, s[26:27]
	s_cbranch_execz .Lcsr_ld_skip15
	global_load_dwordx2 v[58:59], v[18:19], off
.Lcsr_ld_skip15:
	s_mov_b64 exec, -1
.Lcsr_ld_done:
	v_mov_b32_e32 v19, 1
	s_waitcnt vmcnt(0)
	s_cmpk_lt_i32 s33, 0x1
	s_cbranch_scc1 .Lcsr_cnt_done
	v_cmp_lt_i32_e64 s[20:21], -1, v28
	v_bfe_u32 v4, v28, 16, 7
	v_lshlrev_b32_e32 v4, 2, v4
	v_cmp_lt_i32_e64 s[22:23], -1, v30
	v_bfe_u32 v5, v30, 16, 7
	v_lshlrev_b32_e32 v5, 2, v5
	v_cmp_lt_i32_e64 s[24:25], -1, v32
	v_bfe_u32 v6, v32, 16, 7
	v_lshlrev_b32_e32 v6, 2, v6
	v_cmp_lt_i32_e64 s[26:27], -1, v34
	v_bfe_u32 v7, v34, 16, 7
	v_lshlrev_b32_e32 v7, 2, v7
	s_mov_b64 exec, s[20:21]
	ds_add_rtn_u32 v60, v4, v19 offset:37168
	ds_add_f32 v4, v29 offset:38192
	s_mov_b64 exec, s[22:23]
	ds_add_rtn_u32 v61, v5, v19 offset:37168
	ds_add_f32 v5, v31 offset:38192
	s_mov_b64 exec, s[24:25]
	ds_add_rtn_u32 v62, v6, v19 offset:37168
	ds_add_f32 v6, v33 offset:38192
	s_mov_b64 exec, s[26:27]
	ds_add_rtn_u32 v63, v7, v19 offset:37168
	ds_add_f32 v7, v35 offset:38192
	s_mov_b64 exec, -1
	s_cmpk_lt_i32 s33, 0x401
	s_cbranch_scc1 .Lcsr_cnt_done
	v_cmp_lt_i32_e64 s[20:21], -1, v36
	v_bfe_u32 v4, v36, 16, 7
	v_lshlrev_b32_e32 v4, 2, v4
	v_cmp_lt_i32_e64 s[22:23], -1, v38
	v_bfe_u32 v5, v38, 16, 7
	v_lshlrev_b32_e32 v5, 2, v5
	v_cmp_lt_i32_e64 s[24:25], -1, v40
	v_bfe_u32 v6, v40, 16, 7
	v_lshlrev_b32_e32 v6, 2, v6
	v_cmp_lt_i32_e64 s[26:27], -1, v42
	v_bfe_u32 v7, v42, 16, 7
	v_lshlrev_b32_e32 v7, 2, v7
	s_mov_b64 exec, s[20:21]
	ds_add_rtn_u32 v64, v4, v19 offset:37168
	ds_add_f32 v4, v37 offset:38192
	s_mov_b64 exec, s[22:23]
	ds_add_rtn_u32 v65, v5, v19 offset:37168
	ds_add_f32 v5, v39 offset:38192
	s_mov_b64 exec, s[24:25]
	ds_add_rtn_u32 v66, v6, v19 offset:37168
	ds_add_f32 v6, v41 offset:38192
	s_mov_b64 exec, s[26:27]
	ds_add_rtn_u32 v67, v7, v19 offset:37168
	ds_add_f32 v7, v43 offset:38192
	s_mov_b64 exec, -1
	s_cmpk_lt_i32 s33, 0x801
	s_cbranch_scc1 .Lcsr_cnt_done
	v_cmp_lt_i32_e64 s[20:21], -1, v44
	v_bfe_u32 v4, v44, 16, 7
	v_lshlrev_b32_e32 v4, 2, v4
	v_cmp_lt_i32_e64 s[22:23], -1, v46
	v_bfe_u32 v5, v46, 16, 7
	v_lshlrev_b32_e32 v5, 2, v5
	v_cmp_lt_i32_e64 s[24:25], -1, v48
	v_bfe_u32 v6, v48, 16, 7
	v_lshlrev_b32_e32 v6, 2, v6
	v_cmp_lt_i32_e64 s[26:27], -1, v50
	v_bfe_u32 v7, v50, 16, 7
	v_lshlrev_b32_e32 v7, 2, v7
	s_mov_b64 exec, s[20:21]
	ds_add_rtn_u32 v68, v4, v19 offset:37168
	ds_add_f32 v4, v45 offset:38192
	s_mov_b64 exec, s[22:23]
	ds_add_rtn_u32 v69, v5, v19 offset:37168
	ds_add_f32 v5, v47 offset:38192
	s_mov_b64 exec, s[24:25]
	ds_add_rtn_u32 v70, v6, v19 offset:37168
	ds_add_f32 v6, v49 offset:38192
	s_mov_b64 exec, s[26:27]
	ds_add_rtn_u32 v71, v7, v19 offset:37168
	ds_add_f32 v7, v51 offset:38192
	s_mov_b64 exec, -1
	s_cmpk_lt_i32 s33, 0xc01
	s_cbranch_scc1 .Lcsr_cnt_done
	v_cmp_lt_i32_e64 s[20:21], -1, v52
	v_bfe_u32 v4, v52, 16, 7
	v_lshlrev_b32_e32 v4, 2, v4
	v_cmp_lt_i32_e64 s[22:23], -1, v54
	v_bfe_u32 v5, v54, 16, 7
	v_lshlrev_b32_e32 v5, 2, v5
	v_cmp_lt_i32_e64 s[24:25], -1, v56
	v_bfe_u32 v6, v56, 16, 7
	v_lshlrev_b32_e32 v6, 2, v6
	v_cmp_lt_i32_e64 s[26:27], -1, v58
	v_bfe_u32 v7, v58, 16, 7
	v_lshlrev_b32_e32 v7, 2, v7
	s_mov_b64 exec, s[20:21]
	ds_add_rtn_u32 v72, v4, v19 offset:37168
	ds_add_f32 v4, v53 offset:38192
	s_mov_b64 exec, s[22:23]
	ds_add_rtn_u32 v73, v5, v19 offset:37168
	ds_add_f32 v5, v55 offset:38192
	s_mov_b64 exec, s[24:25]
	ds_add_rtn_u32 v74, v6, v19 offset:37168
	ds_add_f32 v6, v57 offset:38192
	s_mov_b64 exec, s[26:27]
	ds_add_rtn_u32 v75, v7, v19 offset:37168
	ds_add_f32 v7, v59 offset:38192
	s_mov_b64 exec, -1
.Lcsr_cnt_done:
	s_waitcnt lgkmcnt(0)
	s_barrier
	v_mov_b32_e32 v5, 0
	s_and_saveexec_b64 s[20:21], s[6:7]
	ds_read_b32 v5, v3 offset:37168
	s_or_b64 exec, exec, s[20:21]
	s_waitcnt lgkmcnt(0)
	ds_bpermute_b32 v6, v20, v5
	s_waitcnt lgkmcnt(0)
	v_cndmask_b32_e64 v6, v6, 0, s[50:51]
	v_add_u32_e32 v6, v6, v5
	ds_bpermute_b32 v7, v21, v6
	s_waitcnt lgkmcnt(0)
	v_cndmask_b32_e64 v7, v7, 0, s[4:5]
	v_add_u32_e32 v6, v7, v6
	ds_bpermute_b32 v7, v22, v6
	s_waitcnt lgkmcnt(0)
	v_cndmask_b32_e64 v7, v7, 0, s[8:9]
	v_add_u32_e32 v6, v7, v6
	ds_bpermute_b32 v7, v23, v6
	s_waitcnt lgkmcnt(0)
	v_cndmask_b32_e64 v7, v7, 0, s[10:11]
	v_add_u32_e32 v6, v7, v6
	ds_bpermute_b32 v7, v24, v6
	s_waitcnt lgkmcnt(0)
	v_cndmask_b32_e64 v7, v7, 0, s[12:13]
	v_add_u32_e32 v6, v7, v6
	ds_bpermute_b32 v7, v25, v6
	s_waitcnt lgkmcnt(0)
	v_cndmask_b32_e64 v7, v7, 0, s[14:15]
	v_add_u32_e32 v6, v7, v6
	s_and_saveexec_b64 s[20:21], s[16:17]
	v_lshlrev_b32_e32 v7, 2, v1
	ds_write_b32 v7, v6 offset:38720
	s_or_b64 exec, exec, s[20:21]
	s_waitcnt lgkmcnt(0)
	s_barrier
	s_and_saveexec_b64 s[20:21], s[6:7]
	ds_read_b32 v7, v27 offset:38720
	v_cmp_eq_u32_e64 s[22:23], 1, v1
	v_sub_u32_e32 v6, v6, v5
	s_waitcnt lgkmcnt(0)
	v_cndmask_b32_e64 v7, 0, v7, s[22:23]
	v_add_u32_e32 v6, v6, v7
	ds_write_b32 v3, v6 offset:36640
	s_or_b64 exec, exec, s[20:21]
	s_and_saveexec_b64 s[20:21], s[0:1]
	ds_write_b32 v27, v26 offset:37152
	s_or_b64 exec, exec, s[20:21]
	s_waitcnt lgkmcnt(0)
	s_barrier
	s_cmpk_lt_i32 s33, 0x1
	s_cbranch_scc1 .Lcsr_sc_done
	v_cmp_lt_i32_e64 s[20:21], -1, v28
	v_bfe_u32 v4, v28, 16, 7
	v_lshlrev_b32_e32 v4, 2, v4
	v_cmp_lt_i32_e64 s[22:23], -1, v30
	v_bfe_u32 v5, v30, 16, 7
	v_lshlrev_b32_e32 v5, 2, v5
	v_cmp_lt_i32_e64 s[24:25], -1, v32
	v_bfe_u32 v6, v32, 16, 7
	v_lshlrev_b32_e32 v6, 2, v6
	v_cmp_lt_i32_e64 s[26:27], -1, v34
	v_bfe_u32 v7, v34, 16, 7
	v_lshlrev_b32_e32 v7, 2, v7
	s_mov_b64 exec, s[20:21]
	ds_read_b32 v4, v4 offset:36640
	s_mov_b64 exec, s[22:23]
	ds_read_b32 v5, v5 offset:36640
	s_mov_b64 exec, s[24:25]
	ds_read_b32 v6, v6 offset:36640
	s_mov_b64 exec, s[26:27]
	ds_read_b32 v7, v7 offset:36640
	s_mov_b64 exec, -1
	s_waitcnt lgkmcnt(3)
	v_add_u32_e32 v4, v4, v60
	v_lshlrev_b32_e32 v4, 3, v4
	s_waitcnt lgkmcnt(2)
	v_add_u32_e32 v5, v5, v61
	v_lshlrev_b32_e32 v5, 3, v5
	s_waitcnt lgkmcnt(1)
	v_add_u32_e32 v6, v6, v62
	v_lshlrev_b32_e32 v6, 3, v6
	s_waitcnt lgkmcnt(0)
	v_add_u32_e32 v7, v7, v63
	v_lshlrev_b32_e32 v7, 3, v7
	s_mov_b64 exec, s[20:21]
	ds_write_b64 v4, v[28:29]
	s_mov_b64 exec, s[22:23]
	ds_write_b64 v5, v[30:31]
	s_mov_b64 exec, s[24:25]
	ds_write_b64 v6, v[32:33]
	s_mov_b64 exec, s[26:27]
	ds_write_b64 v7, v[34:35]
	s_mov_b64 exec, -1
	s_cmpk_lt_i32 s33, 0x401
	s_cbranch_scc1 .Lcsr_sc_done
	v_cmp_lt_i32_e64 s[20:21], -1, v36
	v_bfe_u32 v4, v36, 16, 7
	v_lshlrev_b32_e32 v4, 2, v4
	v_cmp_lt_i32_e64 s[22:23], -1, v38
	v_bfe_u32 v5, v38, 16, 7
	v_lshlrev_b32_e32 v5, 2, v5
	v_cmp_lt_i32_e64 s[24:25], -1, v40
	v_bfe_u32 v6, v40, 16, 7
	v_lshlrev_b32_e32 v6, 2, v6
	v_cmp_lt_i32_e64 s[26:27], -1, v42
	v_bfe_u32 v7, v42, 16, 7
	v_lshlrev_b32_e32 v7, 2, v7
	s_mov_b64 exec, s[20:21]
	ds_read_b32 v4, v4 offset:36640
	s_mov_b64 exec, s[22:23]
	ds_read_b32 v5, v5 offset:36640
	s_mov_b64 exec, s[24:25]
	ds_read_b32 v6, v6 offset:36640
	s_mov_b64 exec, s[26:27]
	ds_read_b32 v7, v7 offset:36640
	s_mov_b64 exec, -1
	s_waitcnt lgkmcnt(3)
	v_add_u32_e32 v4, v4, v64
	v_lshlrev_b32_e32 v4, 3, v4
	s_waitcnt lgkmcnt(2)
	v_add_u32_e32 v5, v5, v65
	v_lshlrev_b32_e32 v5, 3, v5
	s_waitcnt lgkmcnt(1)
	v_add_u32_e32 v6, v6, v66
	v_lshlrev_b32_e32 v6, 3, v6
	s_waitcnt lgkmcnt(0)
	v_add_u32_e32 v7, v7, v67
	v_lshlrev_b32_e32 v7, 3, v7
	s_mov_b64 exec, s[20:21]
	ds_write_b64 v4, v[36:37]
	s_mov_b64 exec, s[22:23]
	ds_write_b64 v5, v[38:39]
	s_mov_b64 exec, s[24:25]
	ds_write_b64 v6, v[40:41]
	s_mov_b64 exec, s[26:27]
	ds_write_b64 v7, v[42:43]
	s_mov_b64 exec, -1
	s_cmpk_lt_i32 s33, 0x801
	s_cbranch_scc1 .Lcsr_sc_done
	v_cmp_lt_i32_e64 s[20:21], -1, v44
	v_bfe_u32 v4, v44, 16, 7
	v_lshlrev_b32_e32 v4, 2, v4
	v_cmp_lt_i32_e64 s[22:23], -1, v46
	v_bfe_u32 v5, v46, 16, 7
	v_lshlrev_b32_e32 v5, 2, v5
	v_cmp_lt_i32_e64 s[24:25], -1, v48
	v_bfe_u32 v6, v48, 16, 7
	v_lshlrev_b32_e32 v6, 2, v6
	v_cmp_lt_i32_e64 s[26:27], -1, v50
	v_bfe_u32 v7, v50, 16, 7
	v_lshlrev_b32_e32 v7, 2, v7
	s_mov_b64 exec, s[20:21]
	ds_read_b32 v4, v4 offset:36640
	s_mov_b64 exec, s[22:23]
	ds_read_b32 v5, v5 offset:36640
	s_mov_b64 exec, s[24:25]
	ds_read_b32 v6, v6 offset:36640
	s_mov_b64 exec, s[26:27]
	ds_read_b32 v7, v7 offset:36640
	s_mov_b64 exec, -1
	s_waitcnt lgkmcnt(3)
	v_add_u32_e32 v4, v4, v68
	v_lshlrev_b32_e32 v4, 3, v4
	s_waitcnt lgkmcnt(2)
	v_add_u32_e32 v5, v5, v69
	v_lshlrev_b32_e32 v5, 3, v5
	s_waitcnt lgkmcnt(1)
	v_add_u32_e32 v6, v6, v70
	v_lshlrev_b32_e32 v6, 3, v6
	s_waitcnt lgkmcnt(0)
	v_add_u32_e32 v7, v7, v71
	v_lshlrev_b32_e32 v7, 3, v7
	s_mov_b64 exec, s[20:21]
	ds_write_b64 v4, v[44:45]
	s_mov_b64 exec, s[22:23]
	ds_write_b64 v5, v[46:47]
	s_mov_b64 exec, s[24:25]
	ds_write_b64 v6, v[48:49]
	s_mov_b64 exec, s[26:27]
	ds_write_b64 v7, v[50:51]
	s_mov_b64 exec, -1
	s_cmpk_lt_i32 s33, 0xc01
	s_cbranch_scc1 .Lcsr_sc_done
	v_cmp_lt_i32_e64 s[20:21], -1, v52
	v_bfe_u32 v4, v52, 16, 7
	v_lshlrev_b32_e32 v4, 2, v4
	v_cmp_lt_i32_e64 s[22:23], -1, v54
	v_bfe_u32 v5, v54, 16, 7
	v_lshlrev_b32_e32 v5, 2, v5
	v_cmp_lt_i32_e64 s[24:25], -1, v56
	v_bfe_u32 v6, v56, 16, 7
	v_lshlrev_b32_e32 v6, 2, v6
	v_cmp_lt_i32_e64 s[26:27], -1, v58
	v_bfe_u32 v7, v58, 16, 7
	v_lshlrev_b32_e32 v7, 2, v7
	s_mov_b64 exec, s[20:21]
	ds_read_b32 v4, v4 offset:36640
	s_mov_b64 exec, s[22:23]
	ds_read_b32 v5, v5 offset:36640
	s_mov_b64 exec, s[24:25]
	ds_read_b32 v6, v6 offset:36640
	s_mov_b64 exec, s[26:27]
	ds_read_b32 v7, v7 offset:36640
	s_mov_b64 exec, -1
	s_waitcnt lgkmcnt(3)
	v_add_u32_e32 v4, v4, v72
	v_lshlrev_b32_e32 v4, 3, v4
	s_waitcnt lgkmcnt(2)
	v_add_u32_e32 v5, v5, v73
	v_lshlrev_b32_e32 v5, 3, v5
	s_waitcnt lgkmcnt(1)
	v_add_u32_e32 v6, v6, v74
	v_lshlrev_b32_e32 v6, 3, v6
	s_waitcnt lgkmcnt(0)
	v_add_u32_e32 v7, v7, v75
	v_lshlrev_b32_e32 v7, 3, v7
	s_mov_b64 exec, s[20:21]
	ds_write_b64 v4, v[52:53]
	s_mov_b64 exec, s[22:23]
	ds_write_b64 v5, v[54:55]
	s_mov_b64 exec, s[24:25]
	ds_write_b64 v6, v[56:57]
	s_mov_b64 exec, s[26:27]
	ds_write_b64 v7, v[58:59]
	s_mov_b64 exec, -1
.Lcsr_sc_done:
	s_waitcnt lgkmcnt(0)
	s_barrier
	s_and_saveexec_b64 s[20:21], s[6:7]
	s_cbranch_execz .Lcsr_rows_done
	v_mov_b32_e32 v1, 0x8f20
	v_lshl_add_u32 v1, v0, 2, v1
	ds_read2_b32 v[6:7], v1 offset1:1
	ds_read_b32 v8, v3 offset:38192
	v_lshl_or_b32 v4, s2, 7, v0
	s_mov_b32 s22, 0xc350
	v_cmp_gt_u32_e32 vcc, s22, v4
	s_waitcnt lgkmcnt(0)
	v_add_f32_e32 v1, 1.0, v8
	s_and_b64 exec, exec, vcc
	s_cbranch_execz .Lcsr_rows_done
	v_mov_b32_e32 v5, 0
	v_lshlrev_b64 v[8:9], 2, v[4:5]
	v_add_u32_e32 v3, v6, v2
	v_lshl_add_u64 v[10:11], s[60:61], 0, v[8:9]
	global_store_dword v[10:11], v3, off
	v_add_u32_e32 v3, v7, v2
	v_lshl_add_u64 v[6:7], s[62:63], 0, v[8:9]
	global_store_dword v[6:7], v3, off
	v_cmp_lt_f32_e32 vcc, 0, v1
	v_mov_b32_e32 v3, v5
	s_and_saveexec_b64 s[22:23], vcc
	s_cbranch_execz .Lcsr_dinv_done
	s_mov_b32 s26, 0xf800000
	v_mul_f32_e32 v3, 0x4f800000, v1
	v_cmp_gt_f32_e32 vcc, s26, v1
	s_nop 1
	v_cndmask_b32_e32 v1, v1, v3, vcc
	v_sqrt_f32_e32 v3, v1
	s_nop 0
	v_add_u32_e32 v6, -1, v3
	v_fma_f32 v7, -v6, v3, v1
	v_cmp_ge_f32_e64 s[24:25], 0, v7
	v_add_u32_e32 v7, 1, v3
	s_nop 0
	v_cndmask_b32_e64 v6, v3, v6, s[24:25]
	v_fma_f32 v3, -v7, v3, v1
	v_cmp_lt_f32_e64 s[24:25], 0, v3
	s_nop 1
	v_cndmask_b32_e64 v3, v6, v7, s[24:25]
	v_mul_f32_e32 v6, 0x37800000, v3
	v_cndmask_b32_e32 v3, v3, v6, vcc
	v_mov_b32_e32 v6, 0x260
	v_cmp_class_f32_e32 vcc, v1, v6
	s_nop 1
	v_cndmask_b32_e32 v1, v3, v1, vcc
	v_div_scale_f32 v3, s[24:25], v1, v1, 1.0
	v_rcp_f32_e32 v6, v3
	s_nop 0
	v_fma_f32 v7, -v3, v6, 1.0
	v_fmac_f32_e32 v6, v7, v6
	v_div_scale_f32 v7, vcc, 1.0, v1, 1.0
	v_mul_f32_e32 v8, v7, v6
	v_fma_f32 v9, -v3, v8, v7
	v_fmac_f32_e32 v8, v9, v6
	v_fma_f32 v3, -v3, v8, v7
	v_div_fmas_f32 v3, v3, v6, v8
	v_div_fixup_f32 v3, v3, v1, 1.0
.Lcsr_dinv_done:
	s_or_b64 exec, exec, s[22:23]
	v_lshl_add_u64 v[4:5], v[4:5], 2, s[56:57]
	global_store_dword v[4:5], v3, off
.Lcsr_rows_done:
	s_mov_b64 exec, -1
	s_cmpk_lt_i32 s33, 0x1
	s_cbranch_scc1 .Lcsr_st_done
	v_mov_b32_e32 v12, v0
	v_cmp_gt_i32_e64 s[20:21], s33, v12
	v_lshlrev_b32_e32 v4, 3, v12
	v_add_u32_e32 v14, 0x100, v0
	v_cmp_gt_i32_e64 s[22:23], s33, v14
	v_lshlrev_b32_e32 v6, 3, v14
	v_add_u32_e32 v16, 0x200, v0
	v_cmp_gt_i32_e64 s[24:25], s33, v16
	v_lshlrev_b32_e32 v8, 3, v16
	v_add_u32_e32 v18, 0x300, v0
	v_cmp_gt_i32_e64 s[26:27], s33, v18
	v_lshlrev_b32_e32 v10, 3, v18
	s_mov_b64 exec, s[20:21]
	ds_read_b64 v[4:5], v4
	s_mov_b64 exec, s[22:23]
	ds_read_b64 v[6:7], v6
	s_mov_b64 exec, s[24:25]
	ds_read_b64 v[8:9], v8
	s_mov_b64 exec, s[26:27]
	ds_read_b64 v[10:11], v10
	s_mov_b64 exec, -1
	v_add_u32_e32 v12, v12, v2
	v_mov_b32_e32 v13, 0
	v_lshl_add_u64 v[12:13], v[12:13], 3, s[54:55]
	v_add_u32_e32 v14, v14, v2
	v_mov_b32_e32 v15, 0
	v_lshl_add_u64 v[14:15], v[14:15], 3, s[54:55]
	v_add_u32_e32 v16, v16, v2
	v_mov_b32_e32 v17, 0
	v_lshl_add_u64 v[16:17], v[16:17], 3, s[54:55]
	v_add_u32_e32 v18, v18, v2
	v_mov_b32_e32 v19, 0
	v_lshl_add_u64 v[18:19], v[18:19], 3, s[54:55]
	s_mov_b64 exec, s[20:21]
	s_cbranch_execz .Lcsr_st_skip0
	s_waitcnt lgkmcnt(3)
	global_store_dwordx2 v[12:13], v[4:5], off sc1
.Lcsr_st_skip0:
	s_mov_b64 exec, s[22:23]
	s_cbranch_execz .Lcsr_st_skip1
	s_waitcnt lgkmcnt(2)
	global_store_dwordx2 v[14:15], v[6:7], off sc1
.Lcsr_st_skip1:
	s_mov_b64 exec, s[24:25]
	s_cbranch_execz .Lcsr_st_skip2
	s_waitcnt lgkmcnt(1)
	global_store_dwordx2 v[16:17], v[8:9], off sc1
.Lcsr_st_skip2:
	s_mov_b64 exec, s[26:27]
	s_cbranch_execz .Lcsr_st_skip3
	s_waitcnt lgkmcnt(0)
	global_store_dwordx2 v[18:19], v[10:11], off sc1
.Lcsr_st_skip3:
	s_mov_b64 exec, -1
	s_waitcnt lgkmcnt(0)
	s_cmpk_lt_i32 s33, 0x401
	s_cbranch_scc1 .Lcsr_st_done
	v_add_u32_e32 v12, 0x400, v0
	v_cmp_gt_i32_e64 s[20:21], s33, v12
	v_lshlrev_b32_e32 v4, 3, v12
	v_add_u32_e32 v14, 0x500, v0
	v_cmp_gt_i32_e64 s[22:23], s33, v14
	v_lshlrev_b32_e32 v6, 3, v14
	v_add_u32_e32 v16, 0x600, v0
	v_cmp_gt_i32_e64 s[24:25], s33, v16
	v_lshlrev_b32_e32 v8, 3, v16
	v_add_u32_e32 v18, 0x700, v0
	v_cmp_gt_i32_e64 s[26:27], s33, v18
	v_lshlrev_b32_e32 v10, 3, v18
	s_mov_b64 exec, s[20:21]
	ds_read_b64 v[4:5], v4
	s_mov_b64 exec, s[22:23]
	ds_read_b64 v[6:7], v6
	s_mov_b64 exec, s[24:25]
	ds_read_b64 v[8:9], v8
	s_mov_b64 exec, s[26:27]
	ds_read_b64 v[10:11], v10
	s_mov_b64 exec, -1
	v_add_u32_e32 v12, v12, v2
	v_mov_b32_e32 v13, 0
	v_lshl_add_u64 v[12:13], v[12:13], 3, s[54:55]
	v_add_u32_e32 v14, v14, v2
	v_mov_b32_e32 v15, 0
	v_lshl_add_u64 v[14:15], v[14:15], 3, s[54:55]
	v_add_u32_e32 v16, v16, v2
	v_mov_b32_e32 v17, 0
	v_lshl_add_u64 v[16:17], v[16:17], 3, s[54:55]
	v_add_u32_e32 v18, v18, v2
	v_mov_b32_e32 v19, 0
	v_lshl_add_u64 v[18:19], v[18:19], 3, s[54:55]
	s_mov_b64 exec, s[20:21]
	s_cbranch_execz .Lcsr_st_skip4
	s_waitcnt lgkmcnt(3)
	global_store_dwordx2 v[12:13], v[4:5], off sc1

.Lcsr_st_skip7:
	s_mov_b64 exec, -1
	s_waitcnt lgkmcnt(0)
	s_cmpk_lt_i32 s33, 0x801
	s_cbranch_scc1 .Lcsr_st_done
	v_add_u32_e32 v12, 0x800, v0
	v_cmp_gt_i32_e64 s[20:21], s33, v12
	v_lshlrev_b32_e32 v4, 3, v12
	v_add_u32_e32 v14, 0x900, v0
	v_cmp_gt_i32_e64 s[22:23], s33, v14
	v_lshlrev_b32_e32 v6, 3, v14
	v_add_u32_e32 v16, 0xa00, v0
	v_cmp_gt_i32_e64 s[24:25], s33, v16
	v_lshlrev_b32_e32 v8, 3, v16
	v_add_u32_e32 v18, 0xb00, v0
	v_cmp_gt_i32_e64 s[26:27], s33, v18
	v_lshlrev_b32_e32 v10, 3, v18
	s_mov_b64 exec, s[20:21]
	ds_read_b64 v[4:5], v4
	s_mov_b64 exec, s[22:23]
	ds_read_b64 v[6:7], v6
	s_mov_b64 exec, s[24:25]
	ds_read_b64 v[8:9], v8
	s_mov_b64 exec, s[26:27]
	ds_read_b64 v[10:11], v10
	s_mov_b64 exec, -1
	v_add_u32_e32 v12, v12, v2
	v_mov_b32_e32 v13, 0
	v_lshl_add_u64 v[12:13], v[12:13], 3, s[54:55]
	v_add_u32_e32 v14, v14, v2
	v_mov_b32_e32 v15, 0
	v_lshl_add_u64 v[14:15], v[14:15], 3, s[54:55]
	v_add_u32_e32 v16, v16, v2
	v_mov_b32_e32 v17, 0
	v_lshl_add_u64 v[16:17], v[16:17], 3, s[54:55]
	v_add_u32_e32 v18, v18, v2
	v_mov_b32_e32 v19, 0
	v_lshl_add_u64 v[18:19], v[18:19], 3, s[54:55]
	s_mov_b64 exec, s[20:21]
	s_cbranch_execz .Lcsr_st_skip8
	s_waitcnt lgkmcnt(3)
	global_store_dwordx2 v[12:13], v[4:5], off sc1

.Lcsr_st_skip11:
	s_mov_b64 exec, -1
	s_waitcnt lgkmcnt(0)
	s_cmpk_lt_i32 s33, 0xc01
	s_cbranch_scc1 .Lcsr_st_done
	v_add_u32_e32 v12, 0xc00, v0
	v_cmp_gt_i32_e64 s[20:21], s33, v12
	v_lshlrev_b32_e32 v4, 3, v12
	v_add_u32_e32 v14, 0xd00, v0
	v_cmp_gt_i32_e64 s[22:23], s33, v14
	v_lshlrev_b32_e32 v6, 3, v14
	v_add_u32_e32 v16, 0xe00, v0
	v_cmp_gt_i32_e64 s[24:25], s33, v16
	v_lshlrev_b32_e32 v8, 3, v16
	v_add_u32_e32 v18, 0xf00, v0
	v_cmp_gt_i32_e64 s[26:27], s33, v18
	v_lshlrev_b32_e32 v10, 3, v18
	s_mov_b64 exec, s[20:21]
	ds_read_b64 v[4:5], v4
	s_mov_b64 exec, s[22:23]
	ds_read_b64 v[6:7], v6
	s_mov_b64 exec, s[24:25]
	ds_read_b64 v[8:9], v8
	s_mov_b64 exec, s[26:27]
	ds_read_b64 v[10:11], v10
	s_mov_b64 exec, -1
	v_add_u32_e32 v12, v12, v2
	v_mov_b32_e32 v13, 0
	v_lshl_add_u64 v[12:13], v[12:13], 3, s[54:55]
	v_add_u32_e32 v14, v14, v2
	v_mov_b32_e32 v15, 0
	v_lshl_add_u64 v[14:15], v[14:15], 3, s[54:55]
	v_add_u32_e32 v16, v16, v2
	v_mov_b32_e32 v17, 0
	v_lshl_add_u64 v[16:17], v[16:17], 3, s[54:55]
	v_add_u32_e32 v18, v18, v2
	v_mov_b32_e32 v19, 0
	v_lshl_add_u64 v[18:19], v[18:19], 3, s[54:55]
	s_mov_b64 exec, s[20:21]
	s_cbranch_execz .Lcsr_st_skip12
	s_waitcnt lgkmcnt(3)
	global_store_dwordx2 v[12:13], v[4:5], off sc1

.Lcsr_st_skip15:
	s_mov_b64 exec, -1
	s_waitcnt lgkmcnt(0)
.Lcsr_st_done:
.LBB1_164:
	s_endpgm
	.p2align	8

	.amdhsa_kernel _Z11k_csr_gemm1PKjPK15HIP_vector_typeIiLj2EEPS2_PiS6_PfS6_PKfPKDv8_DF16_PDF16_
		.amdhsa_group_segment_fixed_size 38736
		.amdhsa_private_segment_fixed_size 0
		.amdhsa_kernarg_size 80
		.amdhsa_user_sgpr_count 2
		.amdhsa_user_sgpr_dispatch_ptr 0
		.amdhsa_user_sgpr_queue_ptr 0
		.amdhsa_user_sgpr_kernarg_segment_ptr 1
		.amdhsa_user_sgpr_dispatch_id 0
		.amdhsa_user_sgpr_kernarg_preload_length 0
		.amdhsa_user_sgpr_kernarg_preload_offset 0
		.amdhsa_user_sgpr_private_segment_size 0
		.amdhsa_uses_dynamic_stack 0
		.amdhsa_enable_private_segment 0
		.amdhsa_system_sgpr_workgroup_id_x 1
		.amdhsa_system_sgpr_workgroup_id_y 0
		.amdhsa_system_sgpr_workgroup_id_z 0
		.amdhsa_system_sgpr_workgroup_info 0
		.amdhsa_system_vgpr_workitem_id 0
		.amdhsa_next_free_vgpr 128
		.amdhsa_next_free_sgpr 96
		.amdhsa_accum_offset 96
		.amdhsa_reserve_vcc 1
		.amdhsa_float_round_mode_32 0
		.amdhsa_float_round_mode_16_64 0
		.amdhsa_float_denorm_mode_32 3
		.amdhsa_float_denorm_mode_16_64 3
		.amdhsa_dx10_clamp 1
		.amdhsa_ieee_mode 1
		.amdhsa_fp16_overflow 0
		.amdhsa_tg_split 0
		.amdhsa_exception_fp_ieee_invalid_op 0
		.amdhsa_exception_fp_denorm_src 0
		.amdhsa_exception_fp_ieee_div_zero 0
		.amdhsa_exception_fp_ieee_overflow 0
		.amdhsa_exception_fp_ieee_underflow 0
		.amdhsa_exception_fp_ieee_inexact 0
		.amdhsa_exception_int_div_zero 0
	.end_amdhsa_kernel

.LBB2_101:
	s_endpgm
	.p2align	8

.LBB4_101:
	s_waitcnt vmcnt(3)
	v_cvt_f32_f16_sdwa v27, v2 dst_sel:DWORD dst_unused:UNUSED_PAD src0_sel:WORD_1
	v_cvt_f32_f16_e32 v26, v2
	v_cvt_f32_f16_sdwa v29, v3 dst_sel:DWORD dst_unused:UNUSED_PAD src0_sel:WORD_1
	v_cvt_f32_f16_e32 v28, v3
	v_lshlrev_b64 v[16:17], 9, v[16:17]
	v_pk_add_f32 v[2:3], v[22:23], v[26:27]
	v_cvt_f32_f16_sdwa v23, v5 dst_sel:DWORD dst_unused:UNUSED_PAD src0_sel:WORD_1
	s_waitcnt vmcnt(0)
	v_pk_fma_f32 v[2:3], v[14:15], v[2:3], v[10:11] op_sel_hi:[0,1,1]
	v_pk_add_f32 v[10:11], v[20:21], v[28:29]
	v_cvt_f32_f16_sdwa v21, v4 dst_sel:DWORD dst_unused:UNUSED_PAD src0_sel:WORD_1
	v_cvt_f32_f16_e32 v20, v4
	v_cvt_f32_f16_e32 v22, v5
	v_lshl_add_u64 v[16:17], s[48:49], 0, v[16:17]
	v_lshlrev_b32_e32 v24, 2, v15
	v_mov_b32_e32 v25, 0
	v_lshl_add_u64 v[16:17], v[16:17], 0, v[24:25]
	v_pk_fma_f32 v[4:5], v[14:15], v[10:11], v[12:13] op_sel_hi:[0,1,1]
	v_pk_add_f32 v[10:11], v[18:19], v[20:21]
	v_pk_add_f32 v[0:1], v[0:1], v[22:23]
	v_pk_fma_f32 v[6:7], v[14:15], v[10:11], v[6:7] op_sel_hi:[0,1,1]
	v_pk_fma_f32 v[8:9], v[14:15], v[0:1], v[8:9] op_sel_hi:[0,1,1]
	global_store_dwordx4 v[16:17], v[2:5], off nt
	global_store_dwordx4 v[16:17], v[6:9], off offset:16 nt
	s_endpgm
	.p2align	8

amdhsa.kernels:
  - .agpr_count:     0
    .args:
      - .actual_access:  read_only
        .address_space:  global
        .offset:         0
        .size:           8
        .value_kind:     global_buffer
      - .actual_access:  read_only
        .address_space:  global
        .offset:         8
        .size:           8
        .value_kind:     global_buffer
      - .actual_access:  read_only
        .address_space:  global
        .offset:         16
        .size:           8
        .value_kind:     global_buffer
      - .actual_access:  read_only
        .address_space:  global
        .offset:         24
        .size:           8
        .value_kind:     global_buffer
      - .actual_access:  read_only
        .address_space:  global
        .offset:         32
        .size:           8
        .value_kind:     global_buffer
      - .actual_access:  write_only
        .address_space:  global
        .offset:         40
        .size:           8
        .value_kind:     global_buffer
      - .actual_access:  write_only
        .address_space:  global
        .offset:         48
        .size:           8
        .value_kind:     global_buffer
      - .actual_access:  write_only
        .address_space:  global
        .offset:         56
        .size:           8
        .value_kind:     global_buffer
      - .actual_access:  write_only
        .address_space:  global
        .offset:         64
        .size:           8
        .value_kind:     global_buffer
    .group_segment_fixed_size: 35168
    .kernarg_segment_align: 8
    .kernarg_segment_size: 72
    .language:       OpenCL C
    .language_version:
      - 2
      - 0
    .max_flat_workgroup_size: 512
    .name:           _Z6k_prepPKiPKfS2_S2_S2_PjP15HIP_vector_typeIiLj2EEPDv8_DF16_Pi
    .private_segment_fixed_size: 0
    .sgpr_count:     46
    .sgpr_spill_count: 0
    .symbol:         _Z6k_prepPKiPKfS2_S2_S2_PjP15HIP_vector_typeIiLj2EEPDv8_DF16_Pi.kd
    .uniform_work_group_size: 1
    .uses_dynamic_stack: false
    .vgpr_count:     58
    .vgpr_spill_count: 0
    .wavefront_size: 64
  - .agpr_count:     32
    .args:
      - .actual_access:  read_only
        .address_space:  global
        .offset:         0
        .size:           8
        .value_kind:     global_buffer
      - .actual_access:  read_only
        .address_space:  global
        .offset:         8
        .size:           8
        .value_kind:     global_buffer
      - .actual_access:  write_only
        .address_space:  global
        .offset:         16
        .size:           8
        .value_kind:     global_buffer
      - .actual_access:  write_only
        .address_space:  global
        .offset:         24
        .size:           8
        .value_kind:     global_buffer
      - .actual_access:  write_only
        .address_space:  global
        .offset:         32
        .size:           8
        .value_kind:     global_buffer
      - .actual_access:  write_only
        .address_space:  global
        .offset:         40
        .size:           8
        .value_kind:     global_buffer
      - .address_space:  global
        .offset:         48
        .size:           8
        .value_kind:     global_buffer
      - .actual_access:  read_only
        .address_space:  global
        .offset:         56
        .size:           8
        .value_kind:     global_buffer
      - .actual_access:  read_only
        .address_space:  global
        .offset:         64
        .size:           8
        .value_kind:     global_buffer
      - .address_space:  global
        .offset:         72
        .size:           8
        .value_kind:     global_buffer
    .group_segment_fixed_size: 38736
    .kernarg_segment_align: 8
    .kernarg_segment_size: 80
    .language:       OpenCL C
    .language_version:
      - 2
      - 0
    .max_flat_workgroup_size: 256
    .name:           _Z11k_csr_gemm1PKjPK15HIP_vector_typeIiLj2EEPS2_PiS6_PfS6_PKfPKDv8_DF16_PDF16_
    .private_segment_fixed_size: 0
    .sgpr_count:     70
    .sgpr_spill_count: 0
    .symbol:         _Z11k_csr_gemm1PKjPK15HIP_vector_typeIiLj2EEPS2_PiS6_PfS6_PKfPKDv8_DF16_PDF16_.kd
    .uniform_work_group_size: 1
    .uses_dynamic_stack: false
    .vgpr_count:     128
    .vgpr_spill_count: 0
    .wavefront_size: 64
  - .agpr_count:     0
    .args:
      - .actual_access:  read_only
        .address_space:  global
        .offset:         0
        .size:           8
        .value_kind:     global_buffer
      - .actual_access:  read_only
        .address_space:  global
        .offset:         8
        .size:           8
        .value_kind:     global_buffer
      - .actual_access:  read_only
        .address_space:  global
        .offset:         16
        .size:           8
        .value_kind:     global_buffer
      - .actual_access:  read_only
        .address_space:  global
        .offset:         24
        .size:           8
        .value_kind:     global_buffer
      - .actual_access:  read_only
        .address_space:  global
        .offset:         32
        .size:           8
        .value_kind:     global_buffer
      - .actual_access:  read_only
        .address_space:  global
        .offset:         40
        .size:           8
        .value_kind:     global_buffer
      - .actual_access:  read_only
        .address_space:  global
        .offset:         48
        .size:           8
        .value_kind:     global_buffer
      - .address_space:  global
        .offset:         56
        .size:           8
        .value_kind:     global_buffer
      - .actual_access:  read_only
        .address_space:  global
        .offset:         64
        .size:           8
        .value_kind:     global_buffer
    .group_segment_fixed_size: 17472
    .kernarg_segment_align: 8
    .kernarg_segment_size: 72
    .language:       OpenCL C
    .language_version:
      - 2
      - 0
    .max_flat_workgroup_size: 256
    .name:           _Z5k_aggILb0ELi4ELb1EEvPK15HIP_vector_typeIjLj4EEPKS0_IiLj2EEPKiS8_PKfSA_PKDv8_DF16_PDF16_Pf
    .private_segment_fixed_size: 0
    .sgpr_count:     75
    .sgpr_spill_count: 0
    .symbol:         _Z5k_aggILb0ELi4ELb1EEvPK15HIP_vector_typeIjLj4EEPKS0_IiLj2EEPKiS8_PKfSA_PKDv8_DF16_PDF16_Pf.kd
    .uniform_work_group_size: 1
    .uses_dynamic_stack: false
    .vgpr_count:     64
    .vgpr_spill_count: 0
    .wavefront_size: 64
  - .agpr_count:     0
    .args:
      - .actual_access:  read_only
        .address_space:  global
        .offset:         0
        .size:           8
        .value_kind:     global_buffer
      - .actual_access:  read_only
        .address_space:  global
        .offset:         8
        .size:           8
        .value_kind:     global_buffer
      - .actual_access:  read_only
        .address_space:  global
        .offset:         16
        .size:           8
        .value_kind:     global_buffer
      - .actual_access:  read_only
        .address_space:  global
        .offset:         24
        .size:           8
        .value_kind:     global_buffer
      - .actual_access:  read_only
        .address_space:  global
        .offset:         32
        .size:           8
        .value_kind:     global_buffer
      - .actual_access:  read_only
        .address_space:  global
        .offset:         40
        .size:           8
        .value_kind:     global_buffer
      - .actual_access:  read_only
        .address_space:  global
        .offset:         48
        .size:           8
        .value_kind:     global_buffer
      - .address_space:  global
        .offset:         56
        .size:           8
        .value_kind:     global_buffer
      - .actual_access:  read_only
        .address_space:  global
        .offset:         64
        .size:           8
        .value_kind:     global_buffer
    .group_segment_fixed_size: 17472
    .kernarg_segment_align: 8
    .kernarg_segment_size: 72
    .language:       OpenCL C
    .language_version:
      - 2
      - 0
    .max_flat_workgroup_size: 256
    .name:           _Z5k_aggILb0ELi4ELb0EEvPK15HIP_vector_typeIjLj4EEPKS0_IiLj2EEPKiS8_PKfSA_PKDv8_DF16_PDF16_Pf
    .private_segment_fixed_size: 0
    .sgpr_count:     75
    .sgpr_spill_count: 0
    .symbol:         _Z5k_aggILb0ELi4ELb0EEvPK15HIP_vector_typeIjLj4EEPKS0_IiLj2EEPKiS8_PKfSA_PKDv8_DF16_PDF16_Pf.kd
    .uniform_work_group_size: 1
    .uses_dynamic_stack: false
    .vgpr_count:     62
    .vgpr_spill_count: 0
    .wavefront_size: 64
  - .agpr_count:     0
    .args:
      - .actual_access:  read_only
        .address_space:  global
        .offset:         0
        .size:           8
        .value_kind:     global_buffer
      - .actual_access:  read_only
        .address_space:  global
        .offset:         8
        .size:           8
        .value_kind:     global_buffer
      - .actual_access:  read_only
        .address_space:  global
        .offset:         16
        .size:           8
        .value_kind:     global_buffer
      - .actual_access:  read_only
        .address_space:  global
        .offset:         24
        .size:           8
        .value_kind:     global_buffer
      - .actual_access:  read_only
        .address_space:  global
        .offset:         32
        .size:           8
        .value_kind:     global_buffer
      - .actual_access:  read_only
        .address_space:  global
        .offset:         40
        .size:           8
        .value_kind:     global_buffer
      - .actual_access:  read_only
        .address_space:  global
        .offset:         48
        .size:           8
        .value_kind:     global_buffer
      - .actual_access:  read_only
        .address_space:  global
        .offset:         56
        .size:           8
        .value_kind:     global_buffer
      - .actual_access:  write_only
        .address_space:  global
        .offset:         64
        .size:           8
        .value_kind:     global_buffer
    .group_segment_fixed_size: 17472
    .kernarg_segment_align: 8
    .kernarg_segment_size: 72
    .language:       OpenCL C
    .language_version:
      - 2
      - 0
    .max_flat_workgroup_size: 256
    .name:           _Z5k_aggILb1ELi4ELb0EEvPK15HIP_vector_typeIjLj4EEPKS0_IiLj2EEPKiS8_PKfSA_PKDv8_DF16_PDF16_Pf
    .private_segment_fixed_size: 0
    .sgpr_count:     73
    .sgpr_spill_count: 0
    .symbol:         _Z5k_aggILb1ELi4ELb0EEvPK15HIP_vector_typeIjLj4EEPKS0_IiLj2EEPKiS8_PKfSA_PKDv8_DF16_PDF16_Pf.kd
    .uniform_work_group_size: 1
    .uses_dynamic_stack: false
    .vgpr_count:     62
    .vgpr_spill_count: 0
    .wavefront_size: 64
